# speedup vs baseline: 1.0229x; 1.0229x over previous
_Z11lstm_kernelPKiPKhPKfS4_S4_Pf:
	s_load_dwordx4 s[12:15], s[0:1], 0x0
	v_readfirstlane_b32 s19, v0
	v_or_b32_e32 v3, 0x400, v0
	s_movk_i32 s4, 0x500
	s_lshr_b32 s7, s19, 6
	s_lshl_b32 s18, s2, 6
	s_mulk_i32 s2, 0x1400
	v_mov_b32_e32 v2, 0x4ff
	v_cmp_gt_u32_e32 vcc, s4, v3
	s_mul_hi_i32 s3, s18, 0x50
	s_waitcnt lgkmcnt(0)
	s_add_u32 s2, s12, s2
	v_cndmask_b32_e32 v2, v2, v3, vcc
	s_addc_u32 s3, s13, s3
	v_lshlrev_b32_e32 v1, 2, v0
	v_lshlrev_b32_e32 v4, 2, v2
	s_movk_i32 s4, 0x184
	v_or_b32_e32 v28, 0x200, v0
	global_load_dword v29, v1, s[2:3]
	global_load_dword v30, v1, s[2:3] offset:2048
	global_load_dword v2, v4, s[2:3]
	v_mov_b32_e32 v4, 0x383
	v_cmp_gt_u32_e32 vcc, s4, v0
	s_add_u32 s2, s14, 0x34000
	s_addc_u32 s3, s15, 0
	v_cndmask_b32_e32 v4, v4, v28, vcc
	v_lshlrev_b32_e32 v31, 4, v0
	v_lshlrev_b32_e32 v4, 4, v4
	global_load_dwordx4 v[6:9], v31, s[2:3]
	global_load_dwordx4 v[10:13], v4, s[2:3]
	v_and_b32_e32 v4, 0x7f, v0
	v_lshlrev_b32_e32 v18, 4, v4
	v_mov_b32_e32 v19, 0
	v_lshl_add_u64 v[4:5], s[14:15], 0, v[18:19]
	s_mov_b32 s2, 0x37000
	v_add_co_u32_e64 v4, s[2:3], s2, v4
	s_nop 1
	v_addc_co_u32_e64 v5, s[2:3], 0, v5, s[2:3]
	global_load_dwordx4 v[14:17], v[4:5], off offset:2112
	s_movk_i32 s22, 0x410
	s_movk_i32 s2, 0x4ff
	v_and_b32_e32 v4, 63, v0
	v_cmp_lt_u32_e64 s[2:3], s2, v3
	s_mul_i32 s5, s7, 0x6000
	s_mul_hi_u32 s4, s7, 0x6000
	s_add_u32 s8, s14, s5
	s_addc_u32 s9, s15, s4
	v_lshlrev_b32_e32 v210, 4, v4
	v_mov_b32_e32 v211, v19
	v_lshl_add_u64 v[20:21], s[8:9], 0, v[210:211]
	s_movk_i32 s4, 0x2000
	v_add_co_u32_e64 v22, s[4:5], s4, v20
	s_nop 1
	v_addc_co_u32_e64 v23, s[4:5], 0, v21, s[4:5]
	s_movk_i32 s4, 0x3000
	s_nop 0
	v_add_co_u32_e64 v24, s[4:5], s4, v20
	global_load_dwordx4 v[90:93], v[22:23], off offset:1024
	global_load_dwordx4 v[86:89], v[22:23], off offset:2048
	v_addc_co_u32_e64 v25, s[4:5], 0, v21, s[4:5]
	s_movk_i32 s4, 0x5000
	s_nop 0
	v_add_co_u32_e64 v26, s[4:5], s4, v20
	s_nop 1
	v_addc_co_u32_e64 v27, s[4:5], 0, v21, s[4:5]
	global_load_dwordx4 v[82:85], v[22:23], off offset:3072
	global_load_dwordx4 v[46:49], v[26:27], off
	global_load_dwordx4 v[42:45], v[26:27], off offset:1024
	global_load_dwordx4 v[38:41], v[26:27], off offset:2048
	global_load_dwordx4 v[94:97], v[24:25], off offset:-4096
	global_load_dwordx4 v[34:37], v[26:27], off offset:3072
	s_movk_i32 s4, 0x1000
	v_add_co_u32_e64 v22, s[4:5], s4, v20
	global_load_dwordx4 v[126:129], v210, s[8:9]
	global_load_dwordx4 v[122:125], v210, s[8:9] offset:1024
	global_load_dwordx4 v[118:121], v210, s[8:9] offset:2048
	global_load_dwordx4 v[114:117], v210, s[8:9] offset:3072
	v_addc_co_u32_e64 v23, s[4:5], 0, v21, s[4:5]
	global_load_dwordx4 v[110:113], v[22:23], off
	global_load_dwordx4 v[106:109], v[22:23], off offset:1024
	global_load_dwordx4 v[102:105], v[22:23], off offset:2048
	global_load_dwordx4 v[98:101], v[22:23], off offset:3072
	global_load_dwordx4 v[78:81], v[24:25], off
	global_load_dwordx4 v[74:77], v[24:25], off offset:1024
	global_load_dwordx4 v[70:73], v[24:25], off offset:2048
	global_load_dwordx4 v[66:69], v[24:25], off offset:3072
	s_movk_i32 s4, 0x4000
	v_add_co_u32_e64 v20, s[4:5], s4, v20
	v_mov_b32_e32 v5, 0x4000
	s_nop 0
	v_addc_co_u32_e64 v21, s[4:5], 0, v21, s[4:5]
	global_load_dwordx4 v[62:65], v[20:21], off
	global_load_dwordx4 v[58:61], v[20:21], off offset:1024
	global_load_dwordx4 v[54:57], v[20:21], off offset:2048
	global_load_dwordx4 v[50:53], v[20:21], off offset:3072
	s_waitcnt vmcnt(26)
	ds_write_b128 v31, v[6:9] offset:16384
	v_lshl_or_b32 v5, v28, 4, v5
	v_add_u32_e32 v6, 0x9840, v31
	v_cndmask_b32_e32 v5, v6, v5, vcc
	s_waitcnt vmcnt(25)
	ds_write_b128 v5, v[10:13]
	s_waitcnt vmcnt(24)
	ds_write_b128 v18, v[14:17] offset:36928
	v_mul_u32_u24_e32 v5, 0xccd, v0
	v_lshrrev_b32_e32 v5, 16, v5
	s_mov_b32 s5, 0xffffec
	v_mul_u32_u24_e32 v6, 0xccd, v28
	s_movk_i32 s4, 0x90
	v_mad_u32_u24 v8, v5, s5, v0
	v_lshlrev_b32_e32 v5, 2, v5
	v_lshrrev_b32_e32 v6, 16, v6
	v_mul_lo_u32 v7, v29, s4
	v_lshl_or_b32 v5, v8, 8, v5
	ds_write_b32 v5, v7 offset:30784
	v_mul_lo_u32 v196, v29, s22
	v_add_u32_e32 v197, 0x24e80, v5
	ds_write_b32 v197, v196
	v_mad_u32_u24 v7, v6, s5, v28
	v_lshlrev_b32_e32 v6, 2, v6
	v_mul_lo_u32 v5, v30, s4
	v_lshl_or_b32 v6, v7, 8, v6
	ds_write_b32 v6, v5 offset:30784
	v_mul_lo_u32 v198, v30, s22
	v_add_u32_e32 v199, 0x24e80, v6
	ds_write_b32 v199, v198
	s_and_saveexec_b64 s[4:5], s[2:3]
	s_xor_b64 s[2:3], exec, s[4:5]
	v_mov_b32_e32 v3, 0x9840
	v_lshl_add_u32 v5, v0, 2, v3
	s_andn2_saveexec_b64 s[2:3], s[2:3]
	v_mul_u32_u24_e32 v5, 0xccd, v3
	s_mov_b32 s4, 0xffffec
	v_mul_u32_u24_sdwa v6, v5, s4 dst_sel:DWORD dst_unused:UNUSED_PAD src0_sel:WORD_1 src1_sel:DWORD
	v_add_lshl_u32 v3, v6, v3, 8
	v_mov_b32_e32 v6, 2
	v_lshlrev_b32_sdwa v5, v6, v5 dst_sel:DWORD dst_unused:UNUSED_PAD src0_sel:DWORD src1_sel:WORD_1
	s_movk_i32 s4, 0x7840
	v_add3_u32 v5, v5, v3, s4
	s_or_b64 exec, exec, s[2:3]
	v_lshrrev_b32_e32 v3, 5, v4
	s_movk_i32 s2, 0x90
	s_lshl_b32 s6, s7, 10
	s_mulk_i32 s7, 0xfd00
	v_and_b32_e32 v182, 31, v0
	v_mul_lo_u32 v200, v2, s22
	v_mul_lo_u32 v2, v2, s2
	s_add_i32 s7, s6, s7
	v_lshlrev_b32_e32 v229, 6, v3
	ds_write_b32 v5, v2
	v_add_u32_e32 v201, 0x1d640, v5
	ds_write_b32 v201, v200
	v_lshlrev_b32_e32 v230, 4, v3
	v_lshlrev_b32_e32 v228, 2, v182
	v_or_b32_e32 v2, s7, v229
	v_mov_b32_e32 v204, 0
	v_mov_b32_e32 v205, 0
	v_mov_b32_e32 v206, 0
	v_mov_b32_e32 v207, 0
	ds_write_b128 v31, v[204:207]
	ds_write_b128 v31, v[204:207] offset:8192
	v_and_b32_e32 v202, 0xfc, v1
	v_add_u32_e32 v202, 0x26280, v202
	ds_write_b32 v202, v204
	s_waitcnt lgkmcnt(0)
	s_barrier
	s_cmpk_lt_u32 s19, 0x100
	s_cbranch_scc1 .Llight_path
	v_add_u32_e32 v3, 0x7800, v228
	ds_read2_b32 v[138:139], v3 offset0:16 offset1:48
	ds_read_b128 v[18:21], v2 offset:36928
	ds_read_b128 v[22:25], v2 offset:36944
	s_waitcnt lgkmcnt(2)
	v_add_u32_e32 v3, v230, v138
	ds_read_b128 v[26:29], v2 offset:36960
	ds_read_b128 v[30:33], v2 offset:36976
	ds_read_b128 v[142:145], v3 offset:16384
	ds_read_b128 v[130:133], v3 offset:16416
	ds_read_b128 v[154:157], v3 offset:16448
	ds_read_b128 v[134:137], v3 offset:16480
	ds_read_b128 v[14:17], v2 offset:37104
	ds_read_b128 v[10:13], v2 offset:37088
	ds_read_b128 v[6:9], v2 offset:37072
	ds_read_b128 v[2:5], v2 offset:37056
	s_waitcnt vmcnt(17) lgkmcnt(7)
	v_mfma_f32_32x32x16_bf16 v[18:33], v[94:97], v[142:145], v[18:33]
	s_waitcnt lgkmcnt(6)
	v_mfma_f32_32x32x16_bf16 v[18:33], v[90:93], v[130:133], v[18:33]
	s_waitcnt lgkmcnt(5)
	v_mfma_f32_32x32x16_bf16 v[18:33], v[86:89], v[154:157], v[18:33]
	s_waitcnt lgkmcnt(4)
	v_mfma_f32_32x32x16_bf16 v[18:33], v[82:85], v[134:137], v[18:33]
	s_cmpk_lt_u32 s19, 0x100
	s_cselect_b64 s[2:3], -1, 0
	s_mov_b64 s[4:5], -1
	s_and_b64 vcc, exec, s[2:3]
	s_cbranch_vccz .LBB1_6
	s_setprio 0
	s_mov_b64 s[4:5], 0

.LBB1_8:
	ds_read_b32 v158, v228 offset:31040
	v_add_u32_e32 v159, v230, v139
	s_nop 2
	v_exp_f32_e32 v139, v20
	v_exp_f32_e32 v138, v24
	v_exp_f32_e32 v141, v28
	v_exp_f32_e32 v140, v32
	v_exp_f32_e32 v18, v18
	v_exp_f32_e32 v20, v22
	v_exp_f32_e32 v22, v26
	v_add_f32_e32 v24, 1.0, v138
	v_add_f32_e32 v26, 1.0, v141
	v_add_f32_e32 v19, 1.0, v139
	v_exp_f32_e32 v23, v30
	v_add_f32_e32 v27, 1.0, v140
	v_fmac_f32_e32 v24, v20, v24
	v_fmac_f32_e32 v26, v22, v26
	v_fmac_f32_e32 v19, v18, v19
	v_fmac_f32_e32 v27, v23, v27
	v_rcp_f32_e32 v18, v24
	v_rcp_f32_e32 v22, v27
	v_rcp_f32_e32 v19, v19
	v_rcp_f32_e32 v23, v26
	v_exp_f32_e32 v146, v21
	v_exp_f32_e32 v147, v25
	s_mov_b32 s8, 0xc038aa3b
	s_mov_b32 s4, 0x4038aa3b
	v_mov_b64_e32 v[160:161], s[8:9]
	v_exp_f32_e32 v148, v29
	v_exp_f32_e32 v149, v33
	v_pk_fma_f32 v[20:21], v[138:139], s[4:5], v[160:161] op_sel_hi:[1,0,0]
	s_nop 0
	v_pk_mul_f32 v[214:215], v[20:21], v[18:19]
	v_pk_fma_f32 v[18:19], v[140:141], s[4:5], v[160:161] op_sel_hi:[1,0,0]
	s_nop 0
	v_pk_mul_f32 v[212:213], v[18:19], v[22:23]
	v_add_u32_e32 v231, s7, v229
	ds_read_b128 v[18:21], v231 offset:36928
	ds_read_b128 v[22:25], v231 offset:36944
	ds_read_b128 v[26:29], v231 offset:36960
	ds_read_b128 v[30:33], v231 offset:36976
	s_waitcnt lgkmcnt(5)
	v_mfma_f32_32x32x16_bf16 v[2:17], v[46:49], v[142:145], v[2:17]
	ds_read_b128 v[138:141], v159 offset:16384
	v_add_f32_e32 v162, 1.0, v146
	v_exp_f32_e32 v163, v215
	v_exp_f32_e32 v164, v214
	v_exp_f32_e32 v165, v213
	v_exp_f32_e32 v166, v212
	v_add_f32_e32 v142, 1.0, v147
	v_add_f32_e32 v143, 1.0, v148
	v_add_f32_e32 v144, 1.0, v149
	v_mfma_f32_32x32x16_bf16 v[2:17], v[42:45], v[130:133], v[2:17]
	ds_read_b128 v[146:149], v159 offset:16416
	v_fmac_f32_e32 v162, v162, v163
	v_fmac_f32_e32 v142, v142, v164
	v_fmac_f32_e32 v143, v143, v165
	v_fmac_f32_e32 v144, v144, v166
	v_mfma_f32_32x32x16_bf16 v[2:17], v[38:41], v[154:157], v[2:17]
	ds_read_b128 v[150:153], v159 offset:16448
	v_rcp_f32_e32 v130, v162
	v_rcp_f32_e32 v131, v142
	v_rcp_f32_e32 v132, v143
	v_rcp_f32_e32 v133, v144
	s_waitcnt vmcnt(16)
	v_mfma_f32_32x32x16_bf16 v[2:17], v[34:37], v[134:137], v[2:17]
	ds_read_b128 v[178:181], v159 offset:16480
	v_fma_f32 v130, -v163, v130, v130
	v_fma_f32 v131, -v164, v131, v131
	v_fma_f32 v132, -v165, v132, v132
	v_fma_f32 v133, -v166, v133, v133
	v_add_u32_e32 v211, s6, v210
	v_cvt_pk_bf16_f32 v130, v130, v131
	v_cvt_pk_bf16_f32 v131, v132, v133
	ds_write_b64 v211, v[130:131]
	s_setprio 0
	s_nop 3
	v_exp_f32_e32 v131, v4
	v_exp_f32_e32 v130, v8
	v_exp_f32_e32 v133, v12
	v_exp_f32_e32 v132, v16
	v_exp_f32_e32 v2, v2
	v_exp_f32_e32 v4, v6
	v_exp_f32_e32 v6, v10
	v_exp_f32_e32 v7, v14
	v_add_f32_e32 v3, 1.0, v131
	v_add_f32_e32 v8, 1.0, v130
	v_add_f32_e32 v10, 1.0, v133
	v_add_f32_e32 v11, 1.0, v132
	v_fmac_f32_e32 v3, v2, v3
	v_fmac_f32_e32 v8, v4, v8
	v_fmac_f32_e32 v10, v6, v10
	v_fmac_f32_e32 v11, v7, v11
	v_rcp_f32_e32 v3, v3
	v_rcp_f32_e32 v2, v8
	v_rcp_f32_e32 v7, v10
	v_rcp_f32_e32 v6, v11
	v_exp_f32_e32 v134, v5
	v_exp_f32_e32 v135, v9
	v_pk_fma_f32 v[4:5], v[130:131], s[4:5], v[160:161] op_sel_hi:[1,0,0]
	v_exp_f32_e32 v130, v13
	v_pk_mul_f32 v[204:205], v[4:5], v[2:3]
	v_pk_fma_f32 v[2:3], v[132:133], s[4:5], v[160:161] op_sel_hi:[1,0,0]
	v_exp_f32_e32 v131, v17
	v_pk_mul_f32 v[202:203], v[2:3], v[6:7]
	ds_read_b128 v[2:5], v231 offset:37056
	ds_read_b128 v[6:9], v231 offset:37072
	ds_read_b128 v[10:13], v231 offset:37088
	ds_read_b128 v[14:17], v231 offset:37104
	s_waitcnt lgkmcnt(8)
	v_mfma_f32_32x32x16_bf16 v[18:33], v[94:97], v[138:141], v[18:33]
	v_add_f32_e32 v132, 1.0, v134
	v_exp_f32_e32 v133, v205
	v_add_f32_e32 v134, 1.0, v135
	v_exp_f32_e32 v135, v204
	v_exp_f32_e32 v136, v203
	v_exp_f32_e32 v137, v202
	v_add_f32_e32 v130, 1.0, v130
	v_add_f32_e32 v131, 1.0, v131
	s_waitcnt lgkmcnt(7)
	v_mfma_f32_32x32x16_bf16 v[18:33], v[90:93], v[146:149], v[18:33]
	v_fmac_f32_e32 v132, v132, v133
	v_fmac_f32_e32 v134, v134, v135
	v_fmac_f32_e32 v130, v130, v136
	v_fmac_f32_e32 v131, v131, v137
	s_waitcnt lgkmcnt(6)
	v_mfma_f32_32x32x16_bf16 v[18:33], v[86:89], v[150:153], v[18:33]
	v_rcp_f32_e32 v132, v132
	v_rcp_f32_e32 v134, v134
	v_rcp_f32_e32 v130, v130
	v_rcp_f32_e32 v131, v131
	s_waitcnt lgkmcnt(5)
	v_mfma_f32_32x32x16_bf16 v[18:33], v[82:85], v[178:181], v[18:33]
	v_fma_f32 v132, -v133, v132, v132
	v_fma_f32 v133, -v135, v134, v134
	v_fma_f32 v134, -v136, v130, v130
	v_fma_f32 v131, -v137, v131, v131
	v_cvt_pk_bf16_f32 v130, v132, v133
	v_cvt_pk_bf16_f32 v131, v134, v131
	ds_write_b64 v211, v[130:131] offset:8
	s_waitcnt lgkmcnt(0)
	s_barrier
	s_mov_b64 s[12:13], -1
	s_and_b64 vcc, exec, s[2:3]
	s_cbranch_vccz .LBB1_10
	s_setprio 0
	s_mov_b64 s[12:13], 0

.LBB1_12:
	ds_read_b32 v194, v228 offset:31168
	ds_read_b128 v[174:177], v210
	v_add_u32_e32 v183, v230, v158
	ds_read_b128 v[170:173], v210 offset:1024
	v_exp_f32_e32 v131, v20
	v_exp_f32_e32 v130, v24
	v_exp_f32_e32 v133, v28
	v_exp_f32_e32 v132, v32
	ds_read_b128 v[166:169], v210 offset:2048
	v_exp_f32_e32 v18, v18
	v_exp_f32_e32 v20, v22
	v_exp_f32_e32 v22, v26
	v_exp_f32_e32 v23, v30
	v_add_f32_e32 v19, 1.0, v131
	v_add_f32_e32 v24, 1.0, v130
	v_add_f32_e32 v26, 1.0, v133
	v_add_f32_e32 v27, 1.0, v132
	ds_read_b128 v[162:165], v210 offset:3072
	v_fmac_f32_e32 v19, v18, v19
	v_fmac_f32_e32 v24, v20, v24
	v_fmac_f32_e32 v26, v22, v26
	v_fmac_f32_e32 v27, v23, v27
	ds_read_b128 v[158:161], v210 offset:4096
	v_rcp_f32_e32 v19, v19
	v_rcp_f32_e32 v18, v24
	v_rcp_f32_e32 v23, v26
	v_rcp_f32_e32 v22, v27
	ds_read_b128 v[154:157], v210 offset:5120
	v_exp_f32_e32 v186, v21
	v_exp_f32_e32 v187, v25
	ds_read_b128 v[142:145], v210 offset:6144
	s_mov_b32 s0, 0xc038aa3b
	s_mov_b32 s12, 0x4038aa3b
	v_mov_b64_e32 v[184:185], s[0:1]
	v_pk_fma_f32 v[20:21], v[130:131], s[12:13], v[184:185] op_sel_hi:[1,0,0]
	v_exp_f32_e32 v188, v29
	v_pk_mul_f32 v[200:201], v[20:21], v[18:19]
	v_pk_fma_f32 v[18:19], v[132:133], s[12:13], v[184:185] op_sel_hi:[1,0,0]
	v_exp_f32_e32 v189, v33
	v_pk_mul_f32 v[198:199], v[18:19], v[22:23]
	ds_read_b128 v[130:133], v210 offset:7168
	ds_read_b128 v[18:21], v231 offset:36928
	ds_read_b128 v[22:25], v231 offset:36944
	ds_read_b128 v[26:29], v231 offset:36960
	ds_read_b128 v[30:33], v231 offset:36976
	v_mfma_f32_32x32x16_bf16 v[2:17], v[46:49], v[138:141], v[2:17]
	ds_read_b128 v[134:137], v183 offset:16384
	v_add_f32_e32 v186, 1.0, v186
	v_exp_f32_e32 v190, v201
	v_exp_f32_e32 v191, v200
	v_exp_f32_e32 v192, v199
	v_exp_f32_e32 v193, v198
	v_add_f32_e32 v187, 1.0, v187
	v_add_f32_e32 v188, 1.0, v188
	v_add_f32_e32 v189, 1.0, v189
	v_mfma_f32_32x32x16_bf16 v[2:17], v[42:45], v[146:149], v[2:17]
	ds_read_b128 v[138:141], v183 offset:16416
	v_fmac_f32_e32 v186, v186, v190
	v_fmac_f32_e32 v187, v187, v191
	v_fmac_f32_e32 v188, v188, v192
	v_fmac_f32_e32 v189, v189, v193
	v_mfma_f32_32x32x16_bf16 v[2:17], v[38:41], v[150:153], v[2:17]
	ds_read_b128 v[146:149], v183 offset:16448
	v_rcp_f32_e32 v186, v186
	v_rcp_f32_e32 v187, v187
	v_rcp_f32_e32 v188, v188
	v_rcp_f32_e32 v189, v189
	v_mfma_f32_32x32x16_bf16 v[2:17], v[34:37], v[178:181], v[2:17]
	ds_read_b128 v[150:153], v183 offset:16480
	v_fma_f32 v183, -v190, v186, v186
	v_fma_f32 v186, -v191, v187, v187
	v_fma_f32 v187, -v192, v188, v188
	v_fma_f32 v188, -v193, v189, v189
	s_waitcnt vmcnt(15) lgkmcnt(0)
	v_mfma_f32_32x32x16_bf16 v[18:33], v[126:129], v[174:177], v[18:33]
	v_cvt_pk_bf16_f32 v178, v183, v186
	v_cvt_pk_bf16_f32 v179, v187, v188
	ds_write_b64 v211, v[178:179] offset:8192
	s_setprio 0
	s_waitcnt vmcnt(14)
	v_mfma_f32_32x32x16_bf16 v[18:33], v[122:125], v[170:173], v[18:33]
	s_nop 0
	v_exp_f32_e32 v179, v4
	v_exp_f32_e32 v178, v8
	v_exp_f32_e32 v181, v12
	v_exp_f32_e32 v180, v16
	s_waitcnt vmcnt(13)
	v_mfma_f32_32x32x16_bf16 v[18:33], v[118:121], v[166:169], v[18:33]
	v_exp_f32_e32 v2, v2
	v_exp_f32_e32 v4, v6
	v_exp_f32_e32 v7, v10
	v_exp_f32_e32 v8, v14
	v_add_f32_e32 v3, 1.0, v179
	v_add_f32_e32 v6, 1.0, v178
	v_add_f32_e32 v10, 1.0, v181
	v_add_f32_e32 v11, 1.0, v180
	s_waitcnt vmcnt(12)
	v_mfma_f32_32x32x16_bf16 v[18:33], v[114:117], v[162:165], v[18:33]
	v_fmac_f32_e32 v3, v2, v3
	v_fmac_f32_e32 v6, v4, v6
	v_fmac_f32_e32 v10, v7, v10
	v_fmac_f32_e32 v11, v8, v11
	s_waitcnt vmcnt(11)
	v_mfma_f32_32x32x16_bf16 v[18:33], v[110:113], v[158:161], v[18:33]
	v_rcp_f32_e32 v3, v3
	v_rcp_f32_e32 v2, v6
	v_rcp_f32_e32 v7, v10
	v_rcp_f32_e32 v6, v11
	s_waitcnt vmcnt(10)
	v_mfma_f32_32x32x16_bf16 v[18:33], v[106:109], v[154:157], v[18:33]
	v_exp_f32_e32 v183, v5
	v_exp_f32_e32 v186, v9
	s_waitcnt vmcnt(9)
	v_mfma_f32_32x32x16_bf16 v[18:33], v[102:105], v[142:145], v[18:33]
	v_fma_f32 v4, v178, s12, v184
	v_fma_f32 v5, v179, s12, v184
	v_exp_f32_e32 v178, v13
	v_pk_mul_f32 v[206:207], v[4:5], v[2:3]
	v_pk_fma_f32 v[2:3], v[180:181], s[12:13], v[184:185] op_sel_hi:[1,0,0]
	v_exp_f32_e32 v179, v17
	v_pk_mul_f32 v[208:209], v[2:3], v[6:7]
	s_waitcnt vmcnt(8)
	v_mfma_f32_32x32x16_bf16 v[18:33], v[98:101], v[130:133], v[18:33]
	ds_read_b128 v[2:5], v231 offset:37056
	ds_read_b128 v[6:9], v231 offset:37072
	ds_read_b128 v[10:13], v231 offset:37088
	ds_read_b128 v[14:17], v231 offset:37104
	v_mfma_f32_32x32x16_bf16 v[18:33], v[94:97], v[134:137], v[18:33]
	v_add_f32_e32 v180, 1.0, v183
	v_exp_f32_e32 v181, v207
	v_add_f32_e32 v183, 1.0, v186
	v_exp_f32_e32 v184, v206
	v_exp_f32_e32 v185, v209
	v_exp_f32_e32 v186, v208
	v_add_f32_e32 v178, 1.0, v178
	v_add_f32_e32 v179, 1.0, v179
	v_mfma_f32_32x32x16_bf16 v[18:33], v[90:93], v[138:141], v[18:33]
	v_fmac_f32_e32 v180, v180, v181
	v_fmac_f32_e32 v183, v183, v184
	v_fmac_f32_e32 v178, v178, v185
	v_fmac_f32_e32 v179, v179, v186
	v_mfma_f32_32x32x16_bf16 v[18:33], v[86:89], v[146:149], v[18:33]
	v_rcp_f32_e32 v180, v180
	v_rcp_f32_e32 v183, v183
	v_rcp_f32_e32 v178, v178
	v_rcp_f32_e32 v179, v179
	v_mfma_f32_32x32x16_bf16 v[18:33], v[82:85], v[150:153], v[18:33]
	v_fma_f32 v180, -v181, v180, v180
	v_fma_f32 v181, -v184, v183, v183
	v_fma_f32 v183, -v185, v178, v178
	v_fma_f32 v179, -v186, v179, v179
	v_cvt_pk_bf16_f32 v178, v180, v181
	v_cvt_pk_bf16_f32 v179, v183, v179
	ds_write_b64 v211, v[178:179] offset:8200
	s_waitcnt lgkmcnt(0)
	s_barrier
	v_mov_b32_e32 v178, 0x7a40
	v_lshl_add_u32 v232, v182, 2, v178
	s_mov_b32 s1, -1
	s_branch .LBB1_14
.LBB1_13:
	v_mfma_f32_32x32x16_bf16 v[2:17], v[78:81], v[206:209], v[2:17]
	ds_read_b32 v194, v232 offset:384
	ds_read_b128 v[174:177], v210
	v_add_u32_e32 v195, v230, v233
	v_mfma_f32_32x32x16_bf16 v[2:17], v[74:77], v[190:193], v[2:17]
	ds_read_b128 v[170:173], v210 offset:1024
	v_exp_f32_e32 v199, v28
	v_exp_f32_e32 v198, v32
	v_exp_f32_e32 v197, v20
	v_exp_f32_e32 v196, v24
	v_mfma_f32_32x32x16_bf16 v[2:17], v[70:73], v[158:161], v[2:17]
	ds_read_b128 v[166:169], v210 offset:2048
	v_exp_f32_e32 v18, v18
	v_exp_f32_e32 v22, v22
	v_exp_f32_e32 v24, v26
	v_exp_f32_e32 v26, v30
	v_add_f32_e32 v20, 1.0, v197
	v_add_f32_e32 v28, 1.0, v196
	v_add_f32_e32 v30, 1.0, v199
	v_add_f32_e32 v32, 1.0, v198
	v_mfma_f32_32x32x16_bf16 v[2:17], v[66:69], v[142:145], v[2:17]
	ds_read_b128 v[162:165], v210 offset:3072
	v_exp_f32_e32 v19, v19
	v_exp_f32_e32 v23, v23
	v_exp_f32_e32 v27, v27
	v_exp_f32_e32 v31, v31
	v_fmac_f32_e32 v20, v18, v20
	v_fmac_f32_e32 v28, v22, v28
	v_fmac_f32_e32 v30, v24, v30
	v_fmac_f32_e32 v32, v26, v32
	v_mfma_f32_32x32x16_bf16 v[2:17], v[62:65], v[154:157], v[2:17]
	ds_read_b128 v[158:161], v210 offset:4096
	v_add_f32_e32 v22, 1.0, v19
	v_rcp_f32_e32 v19, v20
	v_rcp_f32_e32 v18, v28
	v_add_f32_e32 v20, 1.0, v23
	v_rcp_f32_e32 v191, v30
	v_rcp_f32_e32 v190, v32
	v_mfma_f32_32x32x16_bf16 v[2:17], v[58:61], v[182:185], v[2:17]
	ds_read_b128 v[154:157], v210 offset:5120
	v_exp_f32_e32 v206, v21
	v_exp_f32_e32 v207, v25
	v_add_f32_e32 v23, 1.0, v27
	v_rcp_f32_e32 v192, v20
	v_add_f32_e32 v20, 1.0, v31
	v_rcp_f32_e32 v193, v22
	v_mfma_f32_32x32x16_bf16 v[2:17], v[54:57], v[186:189], v[2:17]
	ds_read_b128 v[142:145], v210 offset:6144
	v_exp_f32_e32 v208, v29
	v_exp_f32_e32 v209, v33
	v_rcp_f32_e32 v183, v23
	v_rcp_f32_e32 v182, v20
	v_mfma_f32_32x32x16_bf16 v[2:17], v[50:53], v[134:137], v[2:17]
	v_mov_b64_e32 v[184:185], s[0:1]
	v_fma_f32 v20, v196, s12, v184
	v_fma_f32 v21, v197, s12, v184
	ds_read_b128 v[130:133], v210 offset:7168
	v_mul_f32_e64 v186, v20, v18
	v_mul_f32_e64 v187, v21, v19
	ds_read_b128 v[18:21], v231 offset:36928
	ds_read_b128 v[22:25], v231 offset:36944
	ds_read_b128 v[26:29], v231 offset:36960
	ds_read_b128 v[30:33], v231 offset:36976
	v_pk_fma_f32 v[134:135], v[198:199], s[12:13], v[184:185] op_sel_hi:[1,0,0]
	v_pk_fma_f32 v[200:201], v[192:193], v[220:221], v[186:187]
	v_pk_mul_f32 v[134:135], v[134:135], v[190:191]
	s_nop 0
	v_pk_fma_f32 v[198:199], v[182:183], v[222:223], v[134:135]
	v_mfma_f32_32x32x16_bf16 v[2:17], v[46:49], v[138:141], v[2:17]
	ds_read_b128 v[134:137], v195 offset:16384
	v_add_f32_e32 v182, 1.0, v206
	v_exp_f32_e32 v183, v201
	v_exp_f32_e32 v186, v200
	v_exp_f32_e32 v187, v199
	v_exp_f32_e32 v188, v198
	v_add_f32_e32 v189, 1.0, v207
	v_add_f32_e32 v190, 1.0, v208
	v_add_f32_e32 v191, 1.0, v209
	v_mfma_f32_32x32x16_bf16 v[2:17], v[42:45], v[146:149], v[2:17]
	ds_read_b128 v[138:141], v195 offset:16416
	v_fmac_f32_e32 v182, v182, v183
	v_fmac_f32_e32 v189, v189, v186
	v_fmac_f32_e32 v190, v190, v187
	v_fmac_f32_e32 v191, v191, v188
	v_mfma_f32_32x32x16_bf16 v[2:17], v[38:41], v[150:153], v[2:17]
	ds_read_b128 v[146:149], v195 offset:16448
	v_rcp_f32_e32 v182, v182
	v_rcp_f32_e32 v189, v189
	v_rcp_f32_e32 v190, v190
	v_rcp_f32_e32 v191, v191
	v_mfma_f32_32x32x16_bf16 v[2:17], v[34:37], v[178:181], v[2:17]
	ds_read_b128 v[150:153], v195 offset:16480
	v_fma_f32 v182, -v183, v182, v182
	v_fma_f32 v183, -v186, v189, v189
	v_fma_f32 v186, -v187, v190, v190
	v_fma_f32 v187, -v188, v191, v191
	s_waitcnt lgkmcnt(4)
	v_mfma_f32_32x32x16_bf16 v[18:33], v[126:129], v[174:177], v[18:33]
	v_cvt_pk_bf16_f32 v178, v182, v183
	v_cvt_pk_bf16_f32 v179, v186, v187
	ds_write_b64 v211, v[178:179] offset:8192
	s_setprio 0
	v_mfma_f32_32x32x16_bf16 v[18:33], v[122:125], v[170:173], v[18:33]
	s_nop 1
	v_exp_f32_e32 v179, v4
	v_exp_f32_e32 v178, v8
	v_exp_f32_e32 v181, v12
	v_exp_f32_e32 v180, v16
	v_mfma_f32_32x32x16_bf16 v[18:33], v[118:121], v[166:169], v[18:33]
	v_exp_f32_e32 v2, v2
	v_exp_f32_e32 v6, v6
	v_exp_f32_e32 v10, v10
	v_exp_f32_e32 v12, v14
	v_add_f32_e32 v4, 1.0, v179
	v_add_f32_e32 v8, 1.0, v178
	v_add_f32_e32 v14, 1.0, v181
	v_add_f32_e32 v16, 1.0, v180
	v_mfma_f32_32x32x16_bf16 v[18:33], v[114:117], v[162:165], v[18:33]
	v_exp_f32_e32 v3, v3
	v_fmac_f32_e32 v4, v2, v4
	v_exp_f32_e32 v2, v7
	v_fmac_f32_e32 v8, v6, v8
	v_exp_f32_e32 v6, v11
	v_exp_f32_e32 v7, v15
	v_fmac_f32_e32 v14, v10, v14
	v_fmac_f32_e32 v16, v12, v16
	v_mfma_f32_32x32x16_bf16 v[18:33], v[110:113], v[158:161], v[18:33]
	v_add_f32_e32 v10, 1.0, v3
	v_rcp_f32_e32 v3, v4
	v_add_f32_e32 v4, 1.0, v2
	v_rcp_f32_e32 v2, v8
	v_rcp_f32_e32 v183, v14
	v_rcp_f32_e32 v182, v16
	v_mfma_f32_32x32x16_bf16 v[18:33], v[106:109], v[154:157], v[18:33]
	v_add_f32_e32 v6, 1.0, v6
	v_add_f32_e32 v7, 1.0, v7
	v_rcp_f32_e32 v187, v10
	v_rcp_f32_e32 v186, v4
	v_exp_f32_e32 v190, v5
	v_exp_f32_e32 v191, v9
	v_mfma_f32_32x32x16_bf16 v[18:33], v[102:105], v[142:145], v[18:33]
	v_rcp_f32_e32 v189, v6
	v_rcp_f32_e32 v188, v7
	v_exp_f32_e32 v192, v13
	v_exp_f32_e32 v193, v17
	v_pk_fma_f32 v[4:5], v[178:179], s[12:13], v[184:185] op_sel_hi:[1,0,0]
	v_mfma_f32_32x32x16_bf16 v[18:33], v[98:101], v[130:133], v[18:33]
	v_mul_f32_e64 v178, v4, v2
	v_mul_f32_e64 v179, v5, v3
	ds_read_b128 v[2:5], v231 offset:37056
	ds_read_b128 v[6:9], v231 offset:37072
	ds_read_b128 v[10:13], v231 offset:37088
	ds_read_b128 v[14:17], v231 offset:37104
	v_pk_fma_f32 v[206:207], v[186:187], v[216:217], v[178:179]
	v_pk_fma_f32 v[178:179], v[180:181], s[12:13], v[184:185] op_sel_hi:[1,0,0]
	s_nop 0
	v_pk_mul_f32 v[178:179], v[178:179], v[182:183]
	s_nop 0
	v_pk_fma_f32 v[208:209], v[188:189], v[218:219], v[178:179]
	s_waitcnt lgkmcnt(8)
	v_mfma_f32_32x32x16_bf16 v[18:33], v[94:97], v[134:137], v[18:33]
	v_add_f32_e32 v178, 1.0, v190
	v_exp_f32_e32 v179, v207
	v_add_f32_e32 v180, 1.0, v191
	v_exp_f32_e32 v181, v206
	v_exp_f32_e32 v182, v209
	v_exp_f32_e32 v183, v208
	v_add_f32_e32 v184, 1.0, v192
	v_add_f32_e32 v185, 1.0, v193
	s_waitcnt lgkmcnt(7)
	v_mfma_f32_32x32x16_bf16 v[18:33], v[90:93], v[138:141], v[18:33]
	v_fmac_f32_e32 v178, v178, v179
	v_fmac_f32_e32 v180, v180, v181
	v_fmac_f32_e32 v184, v184, v182
	v_fmac_f32_e32 v185, v185, v183
	s_waitcnt lgkmcnt(6)
	v_mfma_f32_32x32x16_bf16 v[18:33], v[86:89], v[146:149], v[18:33]
	v_rcp_f32_e32 v178, v178
	v_rcp_f32_e32 v180, v180
	v_rcp_f32_e32 v184, v184
	v_rcp_f32_e32 v185, v185
	s_waitcnt lgkmcnt(5)
	v_mfma_f32_32x32x16_bf16 v[18:33], v[82:85], v[150:153], v[18:33]
	v_fma_f32 v178, -v179, v178, v178
	v_fma_f32 v179, -v181, v180, v180
	v_fma_f32 v180, -v182, v184, v184
	v_fma_f32 v181, -v183, v185, v185
	v_cvt_pk_bf16_f32 v178, v178, v179
	v_cvt_pk_bf16_f32 v179, v180, v181
	ds_write_b64 v211, v[178:179] offset:8200
	s_waitcnt lgkmcnt(0)
	s_barrier
	s_add_i32 s1, s1, 2
	s_cmp_gt_u32 s1, 16
	v_add_u32_e32 v232, 0x200, v232
	s_cbranch_scc1 .LBB1_30

.LBB1_18:
	s_waitcnt vmcnt(7)
	v_mfma_f32_32x32x16_bf16 v[2:17], v[78:81], v[174:177], v[2:17]
	v_add_u32_e32 v192, v230, v194
	ds_read_b32 v216, v232
	ds_read_b128 v[194:197], v210 offset:8192
	s_waitcnt vmcnt(6)
	v_mfma_f32_32x32x16_bf16 v[2:17], v[74:77], v[170:173], v[2:17]
	ds_read_b128 v[178:181], v210 offset:9216
	v_exp_f32_e32 v187, v20
	v_exp_f32_e32 v186, v24
	v_exp_f32_e32 v189, v28
	v_exp_f32_e32 v188, v32
	s_waitcnt vmcnt(5)
	v_mfma_f32_32x32x16_bf16 v[2:17], v[70:73], v[166:169], v[2:17]
	ds_read_b128 v[170:173], v210 offset:10240
	v_exp_f32_e32 v18, v18
	v_exp_f32_e32 v22, v22
	v_exp_f32_e32 v24, v26
	v_exp_f32_e32 v26, v30
	v_add_f32_e32 v20, 1.0, v187
	v_add_f32_e32 v28, 1.0, v186
	v_add_f32_e32 v30, 1.0, v189
	v_add_f32_e32 v32, 1.0, v188
	s_waitcnt vmcnt(4)
	v_mfma_f32_32x32x16_bf16 v[2:17], v[66:69], v[162:165], v[2:17]
	ds_read_b128 v[166:169], v210 offset:11264
	v_exp_f32_e32 v19, v19
	v_exp_f32_e32 v23, v23
	v_exp_f32_e32 v27, v27
	v_exp_f32_e32 v31, v31
	v_fmac_f32_e32 v20, v18, v20
	v_fmac_f32_e32 v28, v22, v28
	v_fmac_f32_e32 v30, v24, v30
	v_fmac_f32_e32 v32, v26, v32
	s_waitcnt vmcnt(3)
	v_mfma_f32_32x32x16_bf16 v[2:17], v[62:65], v[158:161], v[2:17]
	ds_read_b128 v[162:165], v210 offset:12288
	v_add_f32_e32 v22, 1.0, v19
	v_rcp_f32_e32 v19, v20
	v_rcp_f32_e32 v18, v28
	v_rcp_f32_e32 v191, v30
	v_rcp_f32_e32 v190, v32
	v_add_f32_e32 v20, 1.0, v23
	s_waitcnt vmcnt(2)
	v_mfma_f32_32x32x16_bf16 v[2:17], v[58:61], v[154:157], v[2:17]
	ds_read_b128 v[174:177], v210 offset:13312
	v_rcp_f32_e32 v159, v22
	v_rcp_f32_e32 v158, v20
	v_exp_f32_e32 v160, v21
	v_exp_f32_e32 v161, v25
	v_add_f32_e32 v23, 1.0, v27
	v_add_f32_e32 v20, 1.0, v31
	s_waitcnt vmcnt(1)
	v_mfma_f32_32x32x16_bf16 v[2:17], v[54:57], v[142:145], v[2:17]
	ds_read_b128 v[182:185], v210 offset:14336
	v_rcp_f32_e32 v155, v23
	v_rcp_f32_e32 v154, v20
	v_exp_f32_e32 v193, v29
	v_exp_f32_e32 v217, v33
	s_waitcnt vmcnt(0)
	v_mfma_f32_32x32x16_bf16 v[2:17], v[50:53], v[130:133], v[2:17]
	v_mov_b64_e32 v[218:219], s[0:1]
	v_fma_f32 v20, v186, s12, v218
	v_fma_f32 v21, v187, s12, v218
	ds_read_b128 v[142:145], v210 offset:15360
	v_mul_f32_e64 v156, v20, v18
	v_mul_f32_e64 v157, v21, v19
	ds_read_b128 v[18:21], v231 offset:36928
	ds_read_b128 v[22:25], v231 offset:36944
	ds_read_b128 v[26:29], v231 offset:36960
	ds_read_b128 v[30:33], v231 offset:36976
	v_pk_fma_f32 v[130:131], v[188:189], s[12:13], v[218:219] op_sel_hi:[1,0,0]
	v_pk_fma_f32 v[214:215], v[158:159], v[214:215], v[156:157]
	v_pk_mul_f32 v[130:131], v[130:131], v[190:191]
	s_nop 0
	v_pk_fma_f32 v[212:213], v[154:155], v[212:213], v[130:131]
	v_mfma_f32_32x32x16_bf16 v[2:17], v[46:49], v[134:137], v[2:17]
	ds_read_b128 v[154:157], v192 offset:16384
	v_add_f32_e32 v130, 1.0, v160
	v_exp_f32_e32 v131, v215
	v_exp_f32_e32 v132, v214
	v_exp_f32_e32 v133, v213
	v_exp_f32_e32 v220, v212
	v_add_f32_e32 v134, 1.0, v161
	v_add_f32_e32 v135, 1.0, v193
	v_add_f32_e32 v136, 1.0, v217
	v_mfma_f32_32x32x16_bf16 v[2:17], v[42:45], v[138:141], v[2:17]
	ds_read_b128 v[158:161], v192 offset:16416
	v_fmac_f32_e32 v130, v130, v131
	v_fmac_f32_e32 v134, v134, v132
	v_fmac_f32_e32 v135, v135, v133
	v_fmac_f32_e32 v136, v136, v220
	v_mfma_f32_32x32x16_bf16 v[2:17], v[38:41], v[146:149], v[2:17]
	ds_read_b128 v[186:189], v192 offset:16448
	v_rcp_f32_e32 v130, v130
	v_rcp_f32_e32 v134, v134
	v_rcp_f32_e32 v135, v135
	v_rcp_f32_e32 v136, v136
	v_mfma_f32_32x32x16_bf16 v[2:17], v[34:37], v[150:153], v[2:17]
	ds_read_b128 v[190:193], v192 offset:16480
	v_fma_f32 v130, -v131, v130, v130
	v_fma_f32 v131, -v132, v134, v134
	v_fma_f32 v132, -v133, v135, v135
	v_fma_f32 v133, -v220, v136, v136
	s_waitcnt lgkmcnt(4)
	v_mfma_f32_32x32x16_bf16 v[18:33], v[126:129], v[194:197], v[18:33]
	v_cvt_pk_bf16_f32 v130, v130, v131
	v_cvt_pk_bf16_f32 v131, v132, v133
	ds_write_b64 v211, v[130:131]
	s_setprio 0
	v_mfma_f32_32x32x16_bf16 v[18:33], v[122:125], v[178:181], v[18:33]
	s_nop 1
	v_exp_f32_e32 v131, v4
	v_exp_f32_e32 v130, v8
	v_exp_f32_e32 v133, v12
	v_exp_f32_e32 v132, v16
	v_mfma_f32_32x32x16_bf16 v[18:33], v[118:121], v[170:173], v[18:33]
	v_exp_f32_e32 v2, v2
	v_exp_f32_e32 v6, v6
	v_exp_f32_e32 v10, v10
	v_exp_f32_e32 v12, v14
	v_add_f32_e32 v4, 1.0, v131
	v_add_f32_e32 v8, 1.0, v130
	v_add_f32_e32 v14, 1.0, v133
	v_add_f32_e32 v16, 1.0, v132
	v_mfma_f32_32x32x16_bf16 v[18:33], v[114:117], v[166:169], v[18:33]
	v_exp_f32_e32 v3, v3
	v_fmac_f32_e32 v4, v2, v4
	v_exp_f32_e32 v2, v7
	v_fmac_f32_e32 v8, v6, v8
	v_exp_f32_e32 v6, v11
	v_exp_f32_e32 v7, v15
	v_fmac_f32_e32 v14, v10, v14
	v_fmac_f32_e32 v16, v12, v16
	v_mfma_f32_32x32x16_bf16 v[18:33], v[110:113], v[162:165], v[18:33]
	v_add_f32_e32 v10, 1.0, v3
	v_rcp_f32_e32 v3, v4
	v_add_f32_e32 v4, 1.0, v2
	v_rcp_f32_e32 v2, v8
	v_rcp_f32_e32 v135, v14
	v_rcp_f32_e32 v134, v16
	v_mfma_f32_32x32x16_bf16 v[18:33], v[106:109], v[174:177], v[18:33]
	v_add_f32_e32 v6, 1.0, v6
	v_add_f32_e32 v7, 1.0, v7
	v_rcp_f32_e32 v137, v10
	v_rcp_f32_e32 v136, v4
	v_exp_f32_e32 v140, v5
	v_exp_f32_e32 v141, v9
	v_mfma_f32_32x32x16_bf16 v[18:33], v[102:105], v[182:185], v[18:33]
	v_rcp_f32_e32 v139, v6
	v_rcp_f32_e32 v138, v7
	v_exp_f32_e32 v146, v13
	v_exp_f32_e32 v147, v17
	v_pk_fma_f32 v[4:5], v[130:131], s[12:13], v[218:219] op_sel_hi:[1,0,0]
	v_mfma_f32_32x32x16_bf16 v[18:33], v[98:101], v[142:145], v[18:33]
	v_mul_f32_e64 v130, v4, v2
	v_mul_f32_e64 v131, v5, v3
	ds_read_b128 v[2:5], v231 offset:37056
	ds_read_b128 v[6:9], v231 offset:37072
	ds_read_b128 v[10:13], v231 offset:37088
	ds_read_b128 v[14:17], v231 offset:37104
	v_pk_fma_f32 v[224:225], v[136:137], v[204:205], v[130:131]
	v_pk_fma_f32 v[130:131], v[132:133], s[12:13], v[218:219] op_sel_hi:[1,0,0]
	s_nop 0
	v_pk_mul_f32 v[130:131], v[130:131], v[134:135]
	s_nop 0
	v_pk_fma_f32 v[226:227], v[138:139], v[202:203], v[130:131]
	s_waitcnt lgkmcnt(8)
	v_mfma_f32_32x32x16_bf16 v[18:33], v[94:97], v[154:157], v[18:33]
	v_add_f32_e32 v130, 1.0, v140
	v_exp_f32_e32 v131, v225
	v_add_f32_e32 v132, 1.0, v141
	v_exp_f32_e32 v133, v224
	v_exp_f32_e32 v134, v227
	v_exp_f32_e32 v135, v226
	v_add_f32_e32 v136, 1.0, v146
	v_add_f32_e32 v137, 1.0, v147
	s_waitcnt lgkmcnt(7)
	v_mfma_f32_32x32x16_bf16 v[18:33], v[90:93], v[158:161], v[18:33]
	v_fmac_f32_e32 v130, v130, v131
	v_fmac_f32_e32 v132, v132, v133
	v_fmac_f32_e32 v136, v136, v134
	v_fmac_f32_e32 v137, v137, v135
	s_waitcnt lgkmcnt(6)
	v_mfma_f32_32x32x16_bf16 v[18:33], v[86:89], v[186:189], v[18:33]
	v_rcp_f32_e32 v130, v130
	v_rcp_f32_e32 v132, v132
	v_rcp_f32_e32 v136, v136
	v_rcp_f32_e32 v137, v137
	s_waitcnt lgkmcnt(5)
	v_mfma_f32_32x32x16_bf16 v[18:33], v[82:85], v[190:193], v[18:33]
	v_fma_f32 v130, -v131, v130, v130
	v_fma_f32 v131, -v133, v132, v132
	v_fma_f32 v132, -v134, v136, v136
	v_fma_f32 v133, -v135, v137, v137
	v_cvt_pk_bf16_f32 v130, v130, v131
	v_cvt_pk_bf16_f32 v131, v132, v133
	ds_write_b64 v211, v[130:131] offset:8
	s_waitcnt lgkmcnt(0)
	s_barrier
	s_mov_b64 s[16:17], -1
	s_and_b64 vcc, exec, s[2:3]
	s_cbranch_vccz .LBB1_20
	s_setprio 0
	s_mov_b64 s[16:17], 0

.LBB1_22:
	v_mfma_f32_32x32x16_bf16 v[2:17], v[78:81], v[194:197], v[2:17]
	ds_read_b32 v233, v232 offset:128
	ds_read_b128 v[202:205], v210
	v_add_u32_e32 v216, v230, v216
	v_mfma_f32_32x32x16_bf16 v[2:17], v[74:77], v[178:181], v[2:17]
	ds_read_b128 v[194:197], v210 offset:1024
	v_exp_f32_e32 v147, v20
	v_exp_f32_e32 v146, v24
	v_exp_f32_e32 v149, v28
	v_exp_f32_e32 v148, v32
	v_mfma_f32_32x32x16_bf16 v[2:17], v[70:73], v[170:173], v[2:17]
	ds_read_b128 v[138:141], v210 offset:2048
	v_exp_f32_e32 v18, v18
	v_exp_f32_e32 v22, v22
	v_exp_f32_e32 v24, v26
	v_exp_f32_e32 v26, v30
	v_add_f32_e32 v20, 1.0, v147
	v_add_f32_e32 v28, 1.0, v146
	v_add_f32_e32 v30, 1.0, v149
	v_add_f32_e32 v32, 1.0, v148
	v_mfma_f32_32x32x16_bf16 v[2:17], v[66:69], v[166:169], v[2:17]
	ds_read_b128 v[134:137], v210 offset:3072
	v_exp_f32_e32 v19, v19
	v_exp_f32_e32 v23, v23
	v_exp_f32_e32 v27, v27
	v_exp_f32_e32 v31, v31
	v_fmac_f32_e32 v20, v18, v20
	v_fmac_f32_e32 v28, v22, v28
	v_fmac_f32_e32 v30, v24, v30
	v_fmac_f32_e32 v32, v26, v32
	v_mfma_f32_32x32x16_bf16 v[2:17], v[62:65], v[162:165], v[2:17]
	ds_read_b128 v[166:169], v210 offset:4096
	v_add_f32_e32 v22, 1.0, v19
	v_rcp_f32_e32 v19, v20
	v_rcp_f32_e32 v18, v28
	v_rcp_f32_e32 v151, v30
	v_rcp_f32_e32 v150, v32
	v_add_f32_e32 v20, 1.0, v23
	v_mfma_f32_32x32x16_bf16 v[2:17], v[58:61], v[174:177], v[2:17]
	ds_read_b128 v[162:165], v210 offset:5120
	v_rcp_f32_e32 v153, v22
	v_rcp_f32_e32 v152, v20
	v_add_f32_e32 v23, 1.0, v27
	v_add_f32_e32 v20, 1.0, v31
	v_exp_f32_e32 v180, v21
	v_exp_f32_e32 v181, v25
	v_mfma_f32_32x32x16_bf16 v[2:17], v[54:57], v[182:185], v[2:17]
	ds_read_b128 v[170:173], v210 offset:6144
	v_rcp_f32_e32 v175, v23
	v_rcp_f32_e32 v174, v20
	v_exp_f32_e32 v176, v29
	v_exp_f32_e32 v177, v33
	v_mfma_f32_32x32x16_bf16 v[2:17], v[50:53], v[142:145], v[2:17]
	v_mov_b64_e32 v[178:179], s[0:1]
	v_fma_f32 v20, v146, s12, v178
	v_fma_f32 v21, v147, s12, v178
	ds_read_b128 v[130:133], v210 offset:7168
	v_mul_f32_e64 v146, v20, v18
	v_mul_f32_e64 v147, v21, v19
	ds_read_b128 v[18:21], v231 offset:36928
	ds_read_b128 v[22:25], v231 offset:36944
	ds_read_b128 v[26:29], v231 offset:36960
	ds_read_b128 v[30:33], v231 offset:36976
	v_pk_fma_f32 v[142:143], v[148:149], s[12:13], v[178:179] op_sel_hi:[1,0,0]
	v_pk_fma_f32 v[220:221], v[152:153], v[200:201], v[146:147]
	v_pk_mul_f32 v[142:143], v[142:143], v[150:151]
	s_nop 0
	v_pk_fma_f32 v[222:223], v[174:175], v[198:199], v[142:143]
	v_mfma_f32_32x32x16_bf16 v[2:17], v[46:49], v[154:157], v[2:17]
	ds_read_b128 v[146:149], v216 offset:16384
	v_add_f32_e32 v142, 1.0, v180
	v_exp_f32_e32 v143, v221
	v_exp_f32_e32 v144, v220
	v_exp_f32_e32 v145, v223
	v_exp_f32_e32 v180, v222
	v_add_f32_e32 v154, 1.0, v181
	v_add_f32_e32 v155, 1.0, v176
	v_add_f32_e32 v156, 1.0, v177
	v_mfma_f32_32x32x16_bf16 v[2:17], v[42:45], v[158:161], v[2:17]
	ds_read_b128 v[150:153], v216 offset:16416
	v_fmac_f32_e32 v142, v142, v143
	v_fmac_f32_e32 v154, v154, v144
	v_fmac_f32_e32 v155, v155, v145
	v_fmac_f32_e32 v156, v156, v180
	v_mfma_f32_32x32x16_bf16 v[2:17], v[38:41], v[186:189], v[2:17]
	ds_read_b128 v[174:177], v216 offset:16448
	v_rcp_f32_e32 v142, v142
	v_rcp_f32_e32 v154, v154
	v_rcp_f32_e32 v155, v155
	v_rcp_f32_e32 v156, v156
	v_mfma_f32_32x32x16_bf16 v[2:17], v[34:37], v[190:193], v[2:17]
	ds_read_b128 v[198:201], v216 offset:16480
	v_fma_f32 v142, -v143, v142, v142
	v_fma_f32 v143, -v144, v154, v154
	v_fma_f32 v144, -v145, v155, v155
	v_fma_f32 v145, -v180, v156, v156
	s_waitcnt lgkmcnt(4)
	v_mfma_f32_32x32x16_bf16 v[18:33], v[126:129], v[202:205], v[18:33]
	v_cvt_pk_bf16_f32 v142, v142, v143
	v_cvt_pk_bf16_f32 v143, v144, v145
	ds_write_b64 v211, v[142:143] offset:8192
	s_setprio 0
	v_mfma_f32_32x32x16_bf16 v[18:33], v[122:125], v[194:197], v[18:33]
	s_nop 1
	v_exp_f32_e32 v143, v4
	v_exp_f32_e32 v142, v8
	v_exp_f32_e32 v145, v12
	v_exp_f32_e32 v144, v16
	v_mfma_f32_32x32x16_bf16 v[18:33], v[118:121], v[138:141], v[18:33]
	v_exp_f32_e32 v2, v2
	v_exp_f32_e32 v6, v6
	v_exp_f32_e32 v10, v10
	v_exp_f32_e32 v12, v14
	v_add_f32_e32 v4, 1.0, v143
	v_add_f32_e32 v8, 1.0, v142
	v_add_f32_e32 v14, 1.0, v145
	v_add_f32_e32 v16, 1.0, v144
	v_mfma_f32_32x32x16_bf16 v[18:33], v[114:117], v[134:137], v[18:33]
	v_exp_f32_e32 v3, v3
	v_fmac_f32_e32 v4, v2, v4
	v_exp_f32_e32 v2, v7
	v_fmac_f32_e32 v8, v6, v8
	v_exp_f32_e32 v6, v11
	v_exp_f32_e32 v7, v15
	v_fmac_f32_e32 v14, v10, v14
	v_fmac_f32_e32 v16, v12, v16
	v_mfma_f32_32x32x16_bf16 v[18:33], v[110:113], v[166:169], v[18:33]
	v_add_f32_e32 v10, 1.0, v3
	v_rcp_f32_e32 v3, v4
	v_add_f32_e32 v4, 1.0, v2
	v_rcp_f32_e32 v2, v8
	v_rcp_f32_e32 v155, v14
	v_rcp_f32_e32 v154, v16
	v_mfma_f32_32x32x16_bf16 v[18:33], v[106:109], v[162:165], v[18:33]
	v_add_f32_e32 v6, 1.0, v6
	v_add_f32_e32 v7, 1.0, v7
	v_rcp_f32_e32 v157, v10
	v_rcp_f32_e32 v156, v4
	v_exp_f32_e32 v160, v5
	v_exp_f32_e32 v161, v9
	v_mfma_f32_32x32x16_bf16 v[18:33], v[102:105], v[170:173], v[18:33]
	v_rcp_f32_e32 v159, v6
	v_rcp_f32_e32 v158, v7
	v_exp_f32_e32 v180, v13
	v_exp_f32_e32 v181, v17
	v_pk_fma_f32 v[4:5], v[142:143], s[12:13], v[178:179] op_sel_hi:[1,0,0]
	v_mfma_f32_32x32x16_bf16 v[18:33], v[98:101], v[130:133], v[18:33]
	v_mul_f32_e64 v142, v4, v2
	v_mul_f32_e64 v143, v5, v3
	ds_read_b128 v[2:5], v231 offset:37056
	ds_read_b128 v[6:9], v231 offset:37072
	ds_read_b128 v[10:13], v231 offset:37088
	ds_read_b128 v[14:17], v231 offset:37104
	v_pk_fma_f32 v[216:217], v[156:157], v[206:207], v[142:143]
	v_pk_fma_f32 v[142:143], v[144:145], s[12:13], v[178:179] op_sel_hi:[1,0,0]
	s_nop 0
	v_pk_mul_f32 v[142:143], v[142:143], v[154:155]
	s_nop 0
	v_pk_fma_f32 v[218:219], v[158:159], v[208:209], v[142:143]
	s_waitcnt lgkmcnt(8)
	v_mfma_f32_32x32x16_bf16 v[18:33], v[94:97], v[146:149], v[18:33]
	v_add_f32_e32 v142, 1.0, v160
	v_exp_f32_e32 v143, v217
	v_add_f32_e32 v144, 1.0, v161
	v_exp_f32_e32 v145, v216
	v_exp_f32_e32 v154, v219
	v_exp_f32_e32 v155, v218
	v_add_f32_e32 v156, 1.0, v180
	v_add_f32_e32 v157, 1.0, v181
	s_waitcnt lgkmcnt(7)
	v_mfma_f32_32x32x16_bf16 v[18:33], v[90:93], v[150:153], v[18:33]
	v_fmac_f32_e32 v142, v142, v143
	v_fmac_f32_e32 v144, v144, v145
	v_fmac_f32_e32 v156, v156, v154
	v_fmac_f32_e32 v157, v157, v155
	s_waitcnt lgkmcnt(6)
	v_mfma_f32_32x32x16_bf16 v[18:33], v[86:89], v[174:177], v[18:33]
	v_rcp_f32_e32 v142, v142
	v_rcp_f32_e32 v144, v144
	v_rcp_f32_e32 v156, v156
	v_rcp_f32_e32 v157, v157
	s_waitcnt lgkmcnt(5)
	v_mfma_f32_32x32x16_bf16 v[18:33], v[82:85], v[198:201], v[18:33]
	v_fma_f32 v142, -v143, v142, v142
	v_fma_f32 v143, -v145, v144, v144
	v_fma_f32 v144, -v154, v156, v156
	v_fma_f32 v145, -v155, v157, v157
	v_cvt_pk_bf16_f32 v142, v142, v143
	v_cvt_pk_bf16_f32 v143, v144, v145
	ds_write_b64 v211, v[142:143] offset:8200
	s_waitcnt lgkmcnt(0)
	s_barrier
	s_mov_b64 s[16:17], -1
	s_and_b64 vcc, exec, s[2:3]
	s_cbranch_vccz .LBB1_24
	s_setprio 0
	s_mov_b64 s[16:17], 0

.LBB1_26:
	v_mfma_f32_32x32x16_bf16 v[2:17], v[78:81], v[202:205], v[2:17]
	v_add_u32_e32 v234, v230, v233
	ds_read_b32 v233, v232 offset:256
	ds_read_b128 v[206:209], v210 offset:8192
	v_mfma_f32_32x32x16_bf16 v[2:17], v[74:77], v[194:197], v[2:17]
	ds_read_b128 v[190:193], v210 offset:9216
	v_exp_f32_e32 v179, v20
	v_exp_f32_e32 v178, v24
	v_exp_f32_e32 v181, v28
	v_exp_f32_e32 v180, v32
	v_mfma_f32_32x32x16_bf16 v[2:17], v[70:73], v[138:141], v[2:17]
	ds_read_b128 v[158:161], v210 offset:10240
	v_exp_f32_e32 v18, v18
	v_exp_f32_e32 v22, v22
	v_exp_f32_e32 v24, v26
	v_exp_f32_e32 v26, v30
	v_add_f32_e32 v20, 1.0, v179
	v_add_f32_e32 v28, 1.0, v178
	v_add_f32_e32 v30, 1.0, v181
	v_add_f32_e32 v32, 1.0, v180
	v_mfma_f32_32x32x16_bf16 v[2:17], v[66:69], v[134:137], v[2:17]
	ds_read_b128 v[142:145], v210 offset:11264
	v_exp_f32_e32 v19, v19
	v_exp_f32_e32 v23, v23
	v_exp_f32_e32 v27, v27
	v_exp_f32_e32 v31, v31
	v_fmac_f32_e32 v20, v18, v20
	v_fmac_f32_e32 v28, v22, v28
	v_fmac_f32_e32 v30, v24, v30
	v_fmac_f32_e32 v32, v26, v32
	v_mfma_f32_32x32x16_bf16 v[2:17], v[62:65], v[166:169], v[2:17]
	ds_read_b128 v[154:157], v210 offset:12288
	v_add_f32_e32 v22, 1.0, v19
	v_rcp_f32_e32 v19, v20
	v_rcp_f32_e32 v18, v28
	v_rcp_f32_e32 v139, v30
	v_rcp_f32_e32 v138, v32
	v_add_f32_e32 v20, 1.0, v23
	v_mfma_f32_32x32x16_bf16 v[2:17], v[58:61], v[162:165], v[2:17]
	ds_read_b128 v[182:185], v210 offset:13312
	v_rcp_f32_e32 v141, v22
	v_rcp_f32_e32 v140, v20
	v_add_f32_e32 v23, 1.0, v27
	v_add_f32_e32 v20, 1.0, v31
	v_exp_f32_e32 v168, v21
	v_exp_f32_e32 v169, v25
	v_mfma_f32_32x32x16_bf16 v[2:17], v[54:57], v[170:173], v[2:17]
	ds_read_b128 v[186:189], v210 offset:14336
	v_rcp_f32_e32 v163, v23
	v_rcp_f32_e32 v162, v20
	v_exp_f32_e32 v194, v29
	v_exp_f32_e32 v195, v33
	v_mfma_f32_32x32x16_bf16 v[2:17], v[50:53], v[130:133], v[2:17]
	v_mov_b64_e32 v[164:165], s[0:1]
	v_fma_f32 v20, v178, s12, v164
	v_fma_f32 v21, v179, s12, v164
	ds_read_b128 v[134:137], v210 offset:15360
	v_mul_f32_e64 v166, v20, v18
	v_mul_f32_e64 v167, v21, v19
	ds_read_b128 v[18:21], v231 offset:36928
	ds_read_b128 v[22:25], v231 offset:36944
	ds_read_b128 v[26:29], v231 offset:36960
	ds_read_b128 v[30:33], v231 offset:36976
	v_pk_fma_f32 v[130:131], v[180:181], s[12:13], v[164:165] op_sel_hi:[1,0,0]
	v_pk_fma_f32 v[214:215], v[140:141], v[214:215], v[166:167]
	v_pk_mul_f32 v[130:131], v[130:131], v[138:139]
	s_nop 0
	v_pk_fma_f32 v[212:213], v[162:163], v[212:213], v[130:131]
	v_mfma_f32_32x32x16_bf16 v[2:17], v[46:49], v[146:149], v[2:17]
	ds_read_b128 v[138:141], v234 offset:16384
	v_add_f32_e32 v130, 1.0, v168
	v_exp_f32_e32 v131, v215
	v_exp_f32_e32 v132, v214
	v_exp_f32_e32 v133, v213
	v_exp_f32_e32 v162, v212
	v_add_f32_e32 v163, 1.0, v169
	v_add_f32_e32 v166, 1.0, v194
	v_add_f32_e32 v167, 1.0, v195
	v_mfma_f32_32x32x16_bf16 v[2:17], v[42:45], v[150:153], v[2:17]
	ds_read_b128 v[146:149], v234 offset:16416
	v_fmac_f32_e32 v130, v130, v131
	v_fmac_f32_e32 v163, v163, v132
	v_fmac_f32_e32 v166, v166, v133
	v_fmac_f32_e32 v167, v167, v162
	v_mfma_f32_32x32x16_bf16 v[2:17], v[38:41], v[174:177], v[2:17]
	ds_read_b128 v[150:153], v234 offset:16448
	v_rcp_f32_e32 v130, v130
	v_rcp_f32_e32 v163, v163
	v_rcp_f32_e32 v166, v166
	v_rcp_f32_e32 v167, v167
	v_mfma_f32_32x32x16_bf16 v[2:17], v[34:37], v[198:201], v[2:17]
	ds_read_b128 v[178:181], v234 offset:16480
	v_fma_f32 v130, -v131, v130, v130
	v_fma_f32 v131, -v132, v163, v163
	v_fma_f32 v132, -v133, v166, v166
	v_fma_f32 v133, -v162, v167, v167
	s_waitcnt lgkmcnt(4)
	v_mfma_f32_32x32x16_bf16 v[18:33], v[126:129], v[206:209], v[18:33]
	v_cvt_pk_bf16_f32 v130, v130, v131
	v_cvt_pk_bf16_f32 v131, v132, v133
	ds_write_b64 v211, v[130:131]
	s_setprio 0
	v_mfma_f32_32x32x16_bf16 v[18:33], v[122:125], v[190:193], v[18:33]
	s_nop 1
	v_exp_f32_e32 v131, v4
	v_exp_f32_e32 v130, v8
	v_exp_f32_e32 v133, v12
	v_exp_f32_e32 v132, v16
	v_mfma_f32_32x32x16_bf16 v[18:33], v[118:121], v[158:161], v[18:33]
	v_exp_f32_e32 v2, v2
	v_exp_f32_e32 v6, v6
	v_exp_f32_e32 v10, v10
	v_exp_f32_e32 v12, v14
	v_add_f32_e32 v4, 1.0, v131
	v_add_f32_e32 v8, 1.0, v130
	v_add_f32_e32 v14, 1.0, v133
	v_add_f32_e32 v16, 1.0, v132
	v_mfma_f32_32x32x16_bf16 v[18:33], v[114:117], v[142:145], v[18:33]
	v_exp_f32_e32 v3, v3
	v_fmac_f32_e32 v4, v2, v4
	v_exp_f32_e32 v2, v7
	v_fmac_f32_e32 v8, v6, v8
	v_exp_f32_e32 v6, v11
	v_exp_f32_e32 v7, v15
	v_fmac_f32_e32 v14, v10, v14
	v_fmac_f32_e32 v16, v12, v16
	v_mfma_f32_32x32x16_bf16 v[18:33], v[110:113], v[154:157], v[18:33]
	v_add_f32_e32 v10, 1.0, v3
	v_rcp_f32_e32 v3, v4
	v_add_f32_e32 v4, 1.0, v2
	v_rcp_f32_e32 v2, v8
	v_rcp_f32_e32 v163, v14
	v_rcp_f32_e32 v162, v16
	v_mfma_f32_32x32x16_bf16 v[18:33], v[106:109], v[182:185], v[18:33]
	v_add_f32_e32 v6, 1.0, v6
	v_add_f32_e32 v7, 1.0, v7
	v_rcp_f32_e32 v167, v10
	v_rcp_f32_e32 v166, v4
	v_exp_f32_e32 v170, v5
	v_exp_f32_e32 v171, v9
	v_mfma_f32_32x32x16_bf16 v[18:33], v[102:105], v[186:189], v[18:33]
	v_rcp_f32_e32 v169, v6
	v_rcp_f32_e32 v168, v7
	v_exp_f32_e32 v172, v13
	v_exp_f32_e32 v173, v17
	v_pk_fma_f32 v[4:5], v[130:131], s[12:13], v[164:165] op_sel_hi:[1,0,0]
	v_mfma_f32_32x32x16_bf16 v[18:33], v[98:101], v[134:137], v[18:33]
	v_mul_f32_e64 v130, v4, v2
	v_mul_f32_e64 v131, v5, v3
	ds_read_b128 v[2:5], v231 offset:37056
	ds_read_b128 v[6:9], v231 offset:37072
	ds_read_b128 v[10:13], v231 offset:37088
	ds_read_b128 v[14:17], v231 offset:37104
	v_pk_fma_f32 v[204:205], v[166:167], v[224:225], v[130:131]
	v_pk_fma_f32 v[130:131], v[132:133], s[12:13], v[164:165] op_sel_hi:[1,0,0]
	s_nop 0
	v_pk_mul_f32 v[130:131], v[130:131], v[162:163]
	s_nop 0
	v_pk_fma_f32 v[202:203], v[168:169], v[226:227], v[130:131]
	s_waitcnt lgkmcnt(8)
	v_mfma_f32_32x32x16_bf16 v[18:33], v[94:97], v[138:141], v[18:33]
	v_add_f32_e32 v130, 1.0, v170
	v_exp_f32_e32 v131, v205
	v_add_f32_e32 v132, 1.0, v171
	v_exp_f32_e32 v133, v204
	v_exp_f32_e32 v162, v203
	v_exp_f32_e32 v163, v202
	v_add_f32_e32 v164, 1.0, v172
	v_add_f32_e32 v165, 1.0, v173
	s_waitcnt lgkmcnt(7)
	v_mfma_f32_32x32x16_bf16 v[18:33], v[90:93], v[146:149], v[18:33]
	v_fmac_f32_e32 v130, v130, v131
	v_fmac_f32_e32 v132, v132, v133
	v_fmac_f32_e32 v164, v164, v162
	v_fmac_f32_e32 v165, v165, v163
	s_waitcnt lgkmcnt(6)
	v_mfma_f32_32x32x16_bf16 v[18:33], v[86:89], v[150:153], v[18:33]
	v_rcp_f32_e32 v130, v130
	v_rcp_f32_e32 v132, v132
	v_rcp_f32_e32 v164, v164
	v_rcp_f32_e32 v165, v165
	s_waitcnt lgkmcnt(5)
	v_mfma_f32_32x32x16_bf16 v[18:33], v[82:85], v[178:181], v[18:33]
	v_fma_f32 v130, -v131, v130, v130
	v_fma_f32 v131, -v133, v132, v132
	v_fma_f32 v132, -v162, v164, v164
	v_fma_f32 v133, -v163, v165, v165
	v_cvt_pk_bf16_f32 v130, v130, v131
	v_cvt_pk_bf16_f32 v131, v132, v133
	ds_write_b64 v211, v[130:131] offset:8
	s_waitcnt lgkmcnt(0)
	s_barrier
	s_mov_b64 s[16:17], -1
	s_and_b64 vcc, exec, s[2:3]
	s_cbranch_vccz .LBB1_28
	s_setprio 0
	s_mov_b64 s[16:17], 0

.Lepilogue:
	s_cmpk_lt_u32 s19, 0x100
	s_cbranch_scc0 .LBB1_40
	s_bfe_u32 s2, s19, 0x10006
	s_lshl_b32 s3, s2, 9
	s_lshl_b32 s0, s2, 13
	s_add_u32 s0, s14, s0
	s_addc_u32 s1, s15, 0
	v_mov_b32_e32 v211, 0
	v_lshl_add_u64 v[6:7], s[0:1], 0, v[210:211]
	v_add_co_u32_e32 v2, vcc, 0x30000, v6
	s_mov_b64 s[0:1], 0x30000
	s_nop 0
	v_addc_co_u32_e32 v3, vcc, 0, v7, vcc
	global_load_dwordx4 v[2:5], v[2:3], off
	v_lshl_add_u64 v[8:9], v[6:7], 0, s[0:1]
	global_load_dwordx4 v[18:21], v[8:9], off offset:1024
	global_load_dwordx4 v[22:25], v[8:9], off offset:2048
	global_load_dwordx4 v[26:29], v[8:9], off offset:3072
	s_mov_b32 s0, 0x31000
	v_add_co_u32_e32 v46, vcc, s0, v6
	s_lshl_b32 s0, s19, 6
	s_nop 0
	v_addc_co_u32_e32 v47, vcc, 0, v7, vcc
	global_load_dwordx4 v[30:33], v[46:47], off
	s_and_b32 s0, s0, 0x2000
	v_or_b32_e32 v58, s0, v210
	ds_read_b128 v[6:9], v58
	ds_read_b128 v[34:37], v58 offset:1024
	global_load_dwordx4 v[38:41], v[46:47], off offset:1024
	v_lshl_or_b32 v62, s2, 7, v230
	s_and_b32 s0, s19, 0x80
	s_or_b32 s0, s3, s0
	s_waitcnt vmcnt(5) lgkmcnt(1)
	v_mfma_f32_32x32x16_bf16 v[2:17], v[2:5], v[6:9], 0
	s_waitcnt vmcnt(4) lgkmcnt(0)
	v_mfma_f32_32x32x16_bf16 v[2:17], v[18:21], v[34:37], v[2:17]
	global_load_dwordx4 v[18:21], v[46:47], off offset:2048
	ds_read_b128 v[34:37], v58 offset:2048
	ds_read_b128 v[42:45], v58 offset:3072
	ds_read_b128 v[50:53], v58 offset:5120
	s_waitcnt vmcnt(4) lgkmcnt(2)
	v_mfma_f32_32x32x16_bf16 v[2:17], v[22:25], v[34:37], v[2:17]
	global_load_dwordx4 v[22:25], v[46:47], off offset:3072
	global_load_dwordx4 v[34:37], v62, s[4:5]
	s_nop 0
	global_load_dwordx4 v[46:49], v62, s[4:5] offset:64
	s_waitcnt vmcnt(6) lgkmcnt(1)
	v_mfma_f32_32x32x16_bf16 v[2:17], v[26:29], v[42:45], v[2:17]
	ds_read_b128 v[42:45], v58 offset:4096
	global_load_dwordx4 v[26:29], v62, s[4:5] offset:32
	s_waitcnt vmcnt(6) lgkmcnt(0)
	v_mfma_f32_32x32x16_bf16 v[2:17], v[30:33], v[42:45], v[2:17]
	global_load_dwordx4 v[30:33], v62, s[4:5] offset:96
	global_load_dwordx4 v[42:45], v62, s[6:7]
	global_load_dwordx4 v[54:57], v62, s[6:7] offset:64
	s_waitcnt vmcnt(8)
	v_mfma_f32_32x32x16_bf16 v[2:17], v[38:41], v[50:53], v[2:17]
	global_load_dwordx4 v[38:41], v62, s[6:7] offset:32
	ds_read_b128 v[50:53], v58 offset:6144
	ds_read_b128 v[58:61], v58 offset:7168
	s_waitcnt vmcnt(8) lgkmcnt(1)
	v_mfma_f32_32x32x16_bf16 v[2:17], v[18:21], v[50:53], v[2:17]
	global_load_dwordx4 v[18:21], v62, s[6:7] offset:96
	v_lshlrev_b32_e32 v50, 2, v229
	s_waitcnt vmcnt(8) lgkmcnt(0)
	v_mfma_f32_32x32x16_bf16 v[2:17], v[22:25], v[58:61], v[2:17]
	s_waitcnt vmcnt(7)
	s_nop 10
	v_add_f32_e32 v2, v2, v34
	v_add_f32_e32 v3, v3, v35
	v_max_f32_e32 v2, 0, v2
	v_add_f32_e32 v4, v4, v36
	v_max_f32_e32 v3, 0, v3
	s_waitcnt vmcnt(3)
	v_fma_f32 v2, v2, v42, 0
	v_add_f32_e32 v5, v5, v37
	v_max_f32_e32 v4, 0, v4
	v_fmac_f32_e32 v2, v3, v43
	v_add_f32_e32 v6, v6, v26
	v_max_f32_e32 v5, 0, v5
	v_fmac_f32_e32 v2, v4, v44
	v_add_f32_e32 v7, v7, v27
	v_max_f32_e32 v6, 0, v6
	v_fmac_f32_e32 v2, v5, v45
	v_add_f32_e32 v8, v8, v28
	v_max_f32_e32 v7, 0, v7
	s_waitcnt vmcnt(1)
	v_fmac_f32_e32 v2, v6, v38
	v_add_f32_e32 v9, v9, v29
	v_max_f32_e32 v8, 0, v8
	v_fmac_f32_e32 v2, v7, v39
	v_add_f32_e32 v10, v10, v46
	v_max_f32_e32 v9, 0, v9
	v_fmac_f32_e32 v2, v8, v40
	v_add_f32_e32 v11, v11, v47
	v_max_f32_e32 v10, 0, v10
	v_fmac_f32_e32 v2, v9, v41
	v_add_f32_e32 v12, v12, v48
	v_max_f32_e32 v11, 0, v11
	v_fmac_f32_e32 v2, v10, v54
	v_add_f32_e32 v13, v13, v49
	v_max_f32_e32 v12, 0, v12
	v_fmac_f32_e32 v2, v11, v55
	v_add_f32_e32 v14, v14, v30
	v_max_f32_e32 v13, 0, v13
	v_fmac_f32_e32 v2, v12, v56
	v_add_f32_e32 v15, v15, v31
	v_max_f32_e32 v14, 0, v14
	v_fmac_f32_e32 v2, v13, v57
	v_add_f32_e32 v16, v16, v32
	v_max_f32_e32 v15, 0, v15
	v_add_f32_e32 v17, v17, v33
	v_max_f32_e32 v16, 0, v16
	v_max_f32_e32 v17, 0, v17
	v_add3_u32 v3, s0, v50, v228
	s_waitcnt vmcnt(0)
	v_fmac_f32_e32 v2, v14, v18
	v_fmac_f32_e32 v2, v15, v19
	v_fmac_f32_e32 v2, v16, v20
	v_fmac_f32_e32 v2, v17, v21
	ds_write_b32 v3, v2 offset:35904

.Llight_path:
	s_waitcnt vmcnt(0)
	v_mul_u32_u24_e32 v236, 36, v228
	v_add_u32_e32 v236, v236, v230
	v_add_u32_e32 v237, s7, v229
	v_mul_u32_u24_e32 v238, 0x104, v228
	v_add_u32_e32 v238, v238, v237
	v_add_u32_e32 v238, 0xb840, v238
	ds_read_b128 v[2:5], v237 offset:36928
	ds_read_b128 v[6:9], v237 offset:36944
	ds_read_b128 v[10:13], v237 offset:36960
	ds_read_b128 v[14:17], v237 offset:36976
	ds_read_b128 v[18:21], v237 offset:37056
	ds_read_b128 v[22:25], v237 offset:37072
	ds_read_b128 v[26:29], v237 offset:37088
	ds_read_b128 v[30:33], v237 offset:37104
	ds_read_b128 v[162:165], v236 offset:16384
	ds_read_b128 v[166:169], v236 offset:16416
	ds_read_b128 v[170:173], v236 offset:16448
	ds_read_b128 v[174:177], v236 offset:16480
	ds_read_b128 v[130:133], v237 offset:36928
	ds_read_b128 v[134:137], v237 offset:36944
	ds_read_b128 v[138:141], v237 offset:36960
	ds_read_b128 v[142:145], v237 offset:36976
	ds_read_b128 v[146:149], v237 offset:37056
	ds_read_b128 v[150:153], v237 offset:37072
	ds_read_b128 v[154:157], v237 offset:37088
	ds_read_b128 v[158:161], v237 offset:37104
	ds_read_b128 v[178:181], v236 offset:20992
	ds_read_b128 v[182:185], v236 offset:21024
	ds_read_b128 v[186:189], v236 offset:21056
	ds_read_b128 v[190:193], v236 offset:21088
	s_waitcnt lgkmcnt(12)
	v_mfma_f32_32x32x16_bf16 v[2:17], v[94:97], v[162:165], v[2:17]
	v_mfma_f32_32x32x16_bf16 v[2:17], v[90:93], v[166:169], v[2:17]
	v_mfma_f32_32x32x16_bf16 v[2:17], v[86:89], v[170:173], v[2:17]
	v_mfma_f32_32x32x16_bf16 v[2:17], v[82:85], v[174:177], v[2:17]
	v_mfma_f32_32x32x16_bf16 v[18:33], v[46:49], v[162:165], v[18:33]
	v_mfma_f32_32x32x16_bf16 v[18:33], v[42:45], v[166:169], v[18:33]
	v_mfma_f32_32x32x16_bf16 v[18:33], v[38:41], v[170:173], v[18:33]
	v_mfma_f32_32x32x16_bf16 v[18:33], v[34:37], v[174:177], v[18:33]
	s_waitcnt lgkmcnt(0)
	v_mfma_f32_32x32x16_bf16 v[130:145], v[94:97], v[178:181], v[130:145]
	v_mfma_f32_32x32x16_bf16 v[130:145], v[90:93], v[182:185], v[130:145]
	v_mfma_f32_32x32x16_bf16 v[130:145], v[86:89], v[186:189], v[130:145]
	v_mfma_f32_32x32x16_bf16 v[130:145], v[82:85], v[190:193], v[130:145]
	v_mfma_f32_32x32x16_bf16 v[146:161], v[46:49], v[178:181], v[146:161]
	v_mfma_f32_32x32x16_bf16 v[146:161], v[42:45], v[182:185], v[146:161]
	v_mfma_f32_32x32x16_bf16 v[146:161], v[38:41], v[186:189], v[146:161]
	v_mfma_f32_32x32x16_bf16 v[146:161], v[34:37], v[190:193], v[146:161]
	s_nop 7
	ds_write_b128 v238, v[2:5] offset:0
	ds_write_b128 v238, v[6:9] offset:16
	ds_write_b128 v238, v[10:13] offset:32
	ds_write_b128 v238, v[14:17] offset:48
	ds_write_b128 v238, v[18:21] offset:128
	ds_write_b128 v238, v[22:25] offset:144
	ds_write_b128 v238, v[26:29] offset:160
	ds_write_b128 v238, v[30:33] offset:176
	s_nop 7
	s_nop 7
	v_add_u32_e32 v239, 0x8200, v238
	ds_write_b128 v239, v[130:133] offset:0
	ds_write_b128 v239, v[134:137] offset:16
	ds_write_b128 v239, v[138:141] offset:32
	ds_write_b128 v239, v[142:145] offset:48
	v_add_u32_e32 v239, 0x8200, v238
	ds_write_b128 v239, v[146:149] offset:128
	ds_write_b128 v239, v[150:153] offset:144
	ds_write_b128 v239, v[154:157] offset:160
	ds_write_b128 v239, v[158:161] offset:176
	s_waitcnt lgkmcnt(0)
	ds_read_b128 v[2:5], v237 offset:36928
	ds_read_b128 v[6:9], v237 offset:36944
	ds_read_b128 v[10:13], v237 offset:36960
	ds_read_b128 v[14:17], v237 offset:36976
	ds_read_b128 v[18:21], v237 offset:37056
	ds_read_b128 v[22:25], v237 offset:37072
	ds_read_b128 v[26:29], v237 offset:37088
	ds_read_b128 v[30:33], v237 offset:37104
	ds_read_b128 v[162:165], v236 offset:25600
	ds_read_b128 v[166:169], v236 offset:25632
	ds_read_b128 v[170:173], v236 offset:25664
	ds_read_b128 v[174:177], v236 offset:25696
	ds_read_b128 v[130:133], v237 offset:36928
	ds_read_b128 v[134:137], v237 offset:36944
	ds_read_b128 v[138:141], v237 offset:36960
	ds_read_b128 v[142:145], v237 offset:36976
	ds_read_b128 v[146:149], v237 offset:37056
	ds_read_b128 v[150:153], v237 offset:37072
	ds_read_b128 v[154:157], v237 offset:37088
	ds_read_b128 v[158:161], v237 offset:37104
	ds_read_b128 v[178:181], v236 offset:30208
	ds_read_b128 v[182:185], v236 offset:30240
	ds_read_b128 v[186:189], v236 offset:30272
	ds_read_b128 v[190:193], v236 offset:30304
	s_waitcnt lgkmcnt(12)
	v_mfma_f32_32x32x16_bf16 v[2:17], v[94:97], v[162:165], v[2:17]
	v_mfma_f32_32x32x16_bf16 v[2:17], v[90:93], v[166:169], v[2:17]
	v_mfma_f32_32x32x16_bf16 v[2:17], v[86:89], v[170:173], v[2:17]
	v_mfma_f32_32x32x16_bf16 v[2:17], v[82:85], v[174:177], v[2:17]
	v_mfma_f32_32x32x16_bf16 v[18:33], v[46:49], v[162:165], v[18:33]
	v_mfma_f32_32x32x16_bf16 v[18:33], v[42:45], v[166:169], v[18:33]
	v_mfma_f32_32x32x16_bf16 v[18:33], v[38:41], v[170:173], v[18:33]
	v_mfma_f32_32x32x16_bf16 v[18:33], v[34:37], v[174:177], v[18:33]
	s_waitcnt lgkmcnt(0)
	v_mfma_f32_32x32x16_bf16 v[130:145], v[94:97], v[178:181], v[130:145]
	v_mfma_f32_32x32x16_bf16 v[130:145], v[90:93], v[182:185], v[130:145]
	v_mfma_f32_32x32x16_bf16 v[130:145], v[86:89], v[186:189], v[130:145]
	v_mfma_f32_32x32x16_bf16 v[130:145], v[82:85], v[190:193], v[130:145]
	v_mfma_f32_32x32x16_bf16 v[146:161], v[46:49], v[178:181], v[146:161]
	v_mfma_f32_32x32x16_bf16 v[146:161], v[42:45], v[182:185], v[146:161]
	v_mfma_f32_32x32x16_bf16 v[146:161], v[38:41], v[186:189], v[146:161]
	v_mfma_f32_32x32x16_bf16 v[146:161], v[34:37], v[190:193], v[146:161]
	s_nop 7
	v_add_u32_e32 v239, 0x10400, v238
	ds_write_b128 v239, v[2:5] offset:0
	ds_write_b128 v239, v[6:9] offset:16
	ds_write_b128 v239, v[10:13] offset:32
	ds_write_b128 v239, v[14:17] offset:48
	v_add_u32_e32 v239, 0x10400, v238
	ds_write_b128 v239, v[18:21] offset:128
	ds_write_b128 v239, v[22:25] offset:144
	ds_write_b128 v239, v[26:29] offset:160
	ds_write_b128 v239, v[30:33] offset:176
	s_nop 7
	s_nop 7
	v_cmp_gt_u32_e32 vcc, 16, v228
	s_and_saveexec_b64 s[20:21], vcc
	v_add_u32_e32 v239, 0x18600, v238
	ds_write_b128 v239, v[130:133] offset:0
	ds_write_b128 v239, v[134:137] offset:16
	ds_write_b128 v239, v[138:141] offset:32
	ds_write_b128 v239, v[142:145] offset:48
	v_add_u32_e32 v239, 0x18600, v238
	ds_write_b128 v239, v[146:149] offset:128
	ds_write_b128 v239, v[150:153] offset:144
	ds_write_b128 v239, v[154:157] offset:160
	ds_write_b128 v239, v[158:161] offset:176
	s_or_b64 exec, exec, s[20:21]
	s_waitcnt lgkmcnt(0)
	s_nop 7
	s_nop 7
	v_add_u32_e32 v231, s7, v229
	v_add_u32_e32 v231, 0xb840, v231
	v_add_u32_e32 v211, s6, v210
	s_mov_b32 s12, 0x4038aa3b
	v_mov_b32_e32 v235, 0xc038aa3b
	s_nop 0
	s_load_dwordx8 s[4:11], s[0:1], 0x10
	s_waitcnt lgkmcnt(0)
	v_add_u32_e32 v232, 0x24e80, v228
	ds_read_b32 v244, v232
	ds_read_b32 v245, v232 offset:128
	ds_read_b128 v[130:133], v210 offset:0
	ds_read_b128 v[134:137], v210 offset:1024
	ds_read_b128 v[138:141], v210 offset:2048
	ds_read_b128 v[142:145], v210 offset:3072
	ds_read_b128 v[146:149], v210 offset:4096
	ds_read_b128 v[150:153], v210 offset:5120
	ds_read_b128 v[154:157], v210 offset:6144
	ds_read_b128 v[158:161], v210 offset:7168
	v_mov_b32_e32 v194, 0
	v_mov_b32_e32 v195, 0
	v_mov_b32_e32 v196, 0
	v_mov_b32_e32 v197, 0
	v_mov_b32_e32 v198, 0
	v_mov_b32_e32 v199, 0
	v_mov_b32_e32 v200, 0
	v_mov_b32_e32 v201, 0
	v_mov_b32_e32 v202, 0
	v_mov_b32_e32 v203, 0
	v_mov_b32_e32 v204, 0
	v_mov_b32_e32 v205, 0
	v_mov_b32_e32 v206, 0
	v_mov_b32_e32 v207, 0
	v_mov_b32_e32 v208, 0
	v_mov_b32_e32 v209, 0
	v_add_u32_e32 v232, 0x100, v232
	s_waitcnt lgkmcnt(8)
	v_add_u32_e32 v233, v231, v244
	v_add_u32_e32 v234, v231, v245
	ds_read_b128 v[2:5], v233 offset:0
	ds_read_b128 v[6:9], v233 offset:16
	ds_read_b128 v[10:13], v233 offset:32
	ds_read_b128 v[14:17], v233 offset:48
	ds_read_b128 v[18:21], v233 offset:128
	ds_read_b128 v[22:25], v233 offset:144
	ds_read_b128 v[26:29], v233 offset:160
	ds_read_b128 v[30:33], v233 offset:176
	ds_read_b128 v[34:37], v234 offset:0
	ds_read_b128 v[38:41], v234 offset:16
	ds_read_b128 v[42:45], v234 offset:32
	ds_read_b128 v[46:49], v234 offset:48
	s_movk_i32 s16, 20
	s_waitcnt lgkmcnt(0)
.Llight_loop:
	v_mfma_f32_32x32x16_bf16 v[18:33], v[78:81], v[130:133], v[18:33]
	ds_read_b128 v[162:165], v210 offset:8192
	ds_read_b128 v[82:85], v234 offset:128
	ds_read_b128 v[86:89], v234 offset:144
	ds_read_b128 v[90:93], v234 offset:160
	ds_read_b128 v[94:97], v234 offset:176
	ds_read_b32 v244, v232 offset:0
	v_exp_f32_e32 v212, v4
	v_exp_f32_e32 v213, v8
	v_exp_f32_e32 v214, v12
	v_exp_f32_e32 v215, v16
	v_mfma_f32_32x32x16_bf16 v[18:33], v[74:77], v[134:137], v[18:33]
	ds_read_b128 v[166:169], v210 offset:9216
	v_exp_f32_e32 v216, v2
	v_exp_f32_e32 v217, v6
	v_exp_f32_e32 v218, v10
	v_exp_f32_e32 v219, v14
	v_add_f32_e32 v236, 1.0, v212
	v_add_f32_e32 v237, 1.0, v213
	v_add_f32_e32 v238, 1.0, v214
	v_add_f32_e32 v239, 1.0, v215
	v_fma_f32 v240, v212, s12, v235
	v_fma_f32 v241, v213, s12, v235
	v_fma_f32 v242, v214, s12, v235
	v_fma_f32 v243, v215, s12, v235
	v_mfma_f32_32x32x16_bf16 v[18:33], v[70:73], v[138:141], v[18:33]
	ds_read_b128 v[170:173], v210 offset:10240
	v_exp_f32_e32 v220, v3
	v_exp_f32_e32 v221, v7
	v_exp_f32_e32 v222, v11
	v_exp_f32_e32 v223, v15
	v_fmac_f32_e32 v236, v216, v236
	v_fmac_f32_e32 v237, v217, v237
	v_fmac_f32_e32 v238, v218, v238
	v_fmac_f32_e32 v239, v219, v239
	v_mfma_f32_32x32x16_bf16 v[18:33], v[66:69], v[142:145], v[18:33]
	ds_read_b128 v[174:177], v210 offset:11264
	v_rcp_f32_e32 v216, v236
	v_rcp_f32_e32 v217, v237
	v_rcp_f32_e32 v218, v238
	v_rcp_f32_e32 v219, v239
	v_add_f32_e32 v220, 1.0, v220
	v_add_f32_e32 v221, 1.0, v221
	v_add_f32_e32 v222, 1.0, v222
	v_add_f32_e32 v223, 1.0, v223
	v_mfma_f32_32x32x16_bf16 v[18:33], v[62:65], v[146:149], v[18:33]
	ds_read_b128 v[178:181], v210 offset:12288
	v_rcp_f32_e32 v220, v220
	v_rcp_f32_e32 v221, v221
	v_rcp_f32_e32 v222, v222
	v_rcp_f32_e32 v223, v223
	v_mul_f32_e32 v240, v240, v216
	v_mul_f32_e32 v241, v241, v217
	v_mul_f32_e32 v242, v242, v218
	v_mul_f32_e32 v243, v243, v219
	v_mfma_f32_32x32x16_bf16 v[18:33], v[58:61], v[150:153], v[18:33]
	ds_read_b128 v[182:185], v210 offset:13312
	v_exp_f32_e32 v224, v5
	v_exp_f32_e32 v225, v9
	v_exp_f32_e32 v226, v13
	v_exp_f32_e32 v227, v17
	v_fma_f32 v194, v220, v194, v240
	v_fma_f32 v195, v221, v195, v241
	v_fma_f32 v196, v222, v196, v242
	v_fma_f32 v197, v223, v197, v243
	v_mfma_f32_32x32x16_bf16 v[18:33], v[54:57], v[154:157], v[18:33]
	ds_read_b128 v[186:189], v210 offset:14336
	v_exp_f32_e32 v212, v194
	v_exp_f32_e32 v213, v195
	v_exp_f32_e32 v214, v196
	v_exp_f32_e32 v215, v197
	v_add_f32_e32 v224, 1.0, v224
	v_add_f32_e32 v225, 1.0, v225
	v_add_f32_e32 v226, 1.0, v226
	v_add_f32_e32 v227, 1.0, v227
	v_fmac_f32_e32 v224, v224, v212
	v_fmac_f32_e32 v225, v225, v213
	v_fmac_f32_e32 v226, v226, v214
	v_fmac_f32_e32 v227, v227, v215
	v_mfma_f32_32x32x16_bf16 v[18:33], v[50:53], v[158:161], v[18:33]
	ds_read_b128 v[190:193], v210 offset:15360
	v_rcp_f32_e32 v224, v224
	v_rcp_f32_e32 v225, v225
	v_rcp_f32_e32 v226, v226
	v_rcp_f32_e32 v227, v227
	v_fma_f32 v224, -v212, v224, v224
	v_fma_f32 v225, -v213, v225, v225
	v_fma_f32 v226, -v214, v226, v226
	v_fma_f32 v227, -v215, v227, v227
	v_cvt_pk_bf16_f32 v224, v224, v225
	v_cvt_pk_bf16_f32 v225, v226, v227
	ds_write_b64 v211, v[224:225] offset:0
	s_waitcnt lgkmcnt(1)
	v_mfma_f32_32x32x16_bf16 v[34:49], v[126:129], v[162:165], v[34:49]
	v_add_u32_e32 v233, v231, v244
	ds_read_b128 v[2:5], v233 offset:0
	ds_read_b128 v[6:9], v233 offset:16
	ds_read_b128 v[10:13], v233 offset:32
	ds_read_b128 v[14:17], v233 offset:48
	v_exp_f32_e32 v212, v20
	v_exp_f32_e32 v213, v24
	v_exp_f32_e32 v214, v28
	v_exp_f32_e32 v215, v32
	v_mfma_f32_32x32x16_bf16 v[34:49], v[122:125], v[166:169], v[34:49]
	v_exp_f32_e32 v216, v18
	v_exp_f32_e32 v217, v22
	v_exp_f32_e32 v218, v26
	v_exp_f32_e32 v219, v30
	v_add_f32_e32 v236, 1.0, v212
	v_add_f32_e32 v237, 1.0, v213
	v_add_f32_e32 v238, 1.0, v214
	v_add_f32_e32 v239, 1.0, v215
	v_fma_f32 v240, v212, s12, v235
	v_fma_f32 v241, v213, s12, v235
	v_fma_f32 v242, v214, s12, v235
	v_fma_f32 v243, v215, s12, v235
	v_mfma_f32_32x32x16_bf16 v[34:49], v[118:121], v[170:173], v[34:49]
	v_exp_f32_e32 v220, v19
	v_exp_f32_e32 v221, v23
	v_exp_f32_e32 v222, v27
	v_exp_f32_e32 v223, v31
	v_fmac_f32_e32 v236, v216, v236
	v_fmac_f32_e32 v237, v217, v237
	v_fmac_f32_e32 v238, v218, v238
	v_fmac_f32_e32 v239, v219, v239
	v_mfma_f32_32x32x16_bf16 v[34:49], v[114:117], v[174:177], v[34:49]
	v_rcp_f32_e32 v216, v236
	v_rcp_f32_e32 v217, v237
	v_rcp_f32_e32 v218, v238
	v_rcp_f32_e32 v219, v239
	v_add_f32_e32 v220, 1.0, v220
	v_add_f32_e32 v221, 1.0, v221
	v_add_f32_e32 v222, 1.0, v222
	v_add_f32_e32 v223, 1.0, v223
	v_mfma_f32_32x32x16_bf16 v[34:49], v[110:113], v[178:181], v[34:49]
	v_rcp_f32_e32 v220, v220
	v_rcp_f32_e32 v221, v221
	v_rcp_f32_e32 v222, v222
	v_rcp_f32_e32 v223, v223
	v_mul_f32_e32 v240, v240, v216
	v_mul_f32_e32 v241, v241, v217
	v_mul_f32_e32 v242, v242, v218
	v_mul_f32_e32 v243, v243, v219
	v_mfma_f32_32x32x16_bf16 v[34:49], v[106:109], v[182:185], v[34:49]
	v_exp_f32_e32 v224, v21
	v_exp_f32_e32 v225, v25
	v_exp_f32_e32 v226, v29
	v_exp_f32_e32 v227, v33
	v_fma_f32 v198, v220, v198, v240
	v_fma_f32 v199, v221, v199, v241
	v_fma_f32 v200, v222, v200, v242
	v_fma_f32 v201, v223, v201, v243
	v_mfma_f32_32x32x16_bf16 v[34:49], v[102:105], v[186:189], v[34:49]
	v_exp_f32_e32 v212, v198
	v_exp_f32_e32 v213, v199
	v_exp_f32_e32 v214, v200
	v_exp_f32_e32 v215, v201
	v_add_f32_e32 v224, 1.0, v224
	v_add_f32_e32 v225, 1.0, v225
	v_add_f32_e32 v226, 1.0, v226
	v_add_f32_e32 v227, 1.0, v227
	v_fmac_f32_e32 v224, v224, v212
	v_fmac_f32_e32 v225, v225, v213
	v_fmac_f32_e32 v226, v226, v214
	v_fmac_f32_e32 v227, v227, v215
	v_mfma_f32_32x32x16_bf16 v[34:49], v[98:101], v[190:193], v[34:49]
	v_rcp_f32_e32 v224, v224
	v_rcp_f32_e32 v225, v225
	v_rcp_f32_e32 v226, v226
	v_rcp_f32_e32 v227, v227
	v_fma_f32 v224, -v212, v224, v224
	v_fma_f32 v225, -v213, v225, v225
	v_fma_f32 v226, -v214, v226, v226
	v_fma_f32 v227, -v215, v227, v227
	v_cvt_pk_bf16_f32 v224, v224, v225
	v_cvt_pk_bf16_f32 v225, v226, v227
	ds_write_b64 v211, v[224:225] offset:8
	s_waitcnt lgkmcnt(0)
	s_barrier
	v_mfma_f32_32x32x16_bf16 v[82:97], v[78:81], v[162:165], v[82:97]
	ds_read_b128 v[130:133], v210 offset:0
	ds_read_b128 v[18:21], v233 offset:128
	ds_read_b128 v[22:25], v233 offset:144
	ds_read_b128 v[26:29], v233 offset:160
	ds_read_b128 v[30:33], v233 offset:176
	ds_read_b32 v245, v232 offset:128
	v_exp_f32_e32 v212, v36
	v_exp_f32_e32 v213, v40
	v_exp_f32_e32 v214, v44
	v_exp_f32_e32 v215, v48
	v_mfma_f32_32x32x16_bf16 v[82:97], v[74:77], v[166:169], v[82:97]
	ds_read_b128 v[134:137], v210 offset:1024
	v_exp_f32_e32 v216, v34
	v_exp_f32_e32 v217, v38
	v_exp_f32_e32 v218, v42
	v_exp_f32_e32 v219, v46
	v_add_f32_e32 v236, 1.0, v212
	v_add_f32_e32 v237, 1.0, v213
	v_add_f32_e32 v238, 1.0, v214
	v_add_f32_e32 v239, 1.0, v215
	v_fma_f32 v240, v212, s12, v235
	v_fma_f32 v241, v213, s12, v235
	v_fma_f32 v242, v214, s12, v235
	v_fma_f32 v243, v215, s12, v235
	v_mfma_f32_32x32x16_bf16 v[82:97], v[70:73], v[170:173], v[82:97]
	ds_read_b128 v[138:141], v210 offset:2048
	v_exp_f32_e32 v220, v35
	v_exp_f32_e32 v221, v39
	v_exp_f32_e32 v222, v43
	v_exp_f32_e32 v223, v47
	v_fmac_f32_e32 v236, v216, v236
	v_fmac_f32_e32 v237, v217, v237
	v_fmac_f32_e32 v238, v218, v238
	v_fmac_f32_e32 v239, v219, v239
	v_mfma_f32_32x32x16_bf16 v[82:97], v[66:69], v[174:177], v[82:97]
	ds_read_b128 v[142:145], v210 offset:3072
	v_rcp_f32_e32 v216, v236
	v_rcp_f32_e32 v217, v237
	v_rcp_f32_e32 v218, v238
	v_rcp_f32_e32 v219, v239
	v_add_f32_e32 v220, 1.0, v220
	v_add_f32_e32 v221, 1.0, v221
	v_add_f32_e32 v222, 1.0, v222
	v_add_f32_e32 v223, 1.0, v223
	v_mfma_f32_32x32x16_bf16 v[82:97], v[62:65], v[178:181], v[82:97]
	ds_read_b128 v[146:149], v210 offset:4096
	v_rcp_f32_e32 v220, v220
	v_rcp_f32_e32 v221, v221
	v_rcp_f32_e32 v222, v222
	v_rcp_f32_e32 v223, v223
	v_mul_f32_e32 v240, v240, v216
	v_mul_f32_e32 v241, v241, v217
	v_mul_f32_e32 v242, v242, v218
	v_mul_f32_e32 v243, v243, v219
	v_mfma_f32_32x32x16_bf16 v[82:97], v[58:61], v[182:185], v[82:97]
	ds_read_b128 v[150:153], v210 offset:5120
	v_exp_f32_e32 v224, v37
	v_exp_f32_e32 v225, v41
	v_exp_f32_e32 v226, v45
	v_exp_f32_e32 v227, v49
	v_fma_f32 v202, v220, v202, v240
	v_fma_f32 v203, v221, v203, v241
	v_fma_f32 v204, v222, v204, v242
	v_fma_f32 v205, v223, v205, v243
	v_mfma_f32_32x32x16_bf16 v[82:97], v[54:57], v[186:189], v[82:97]
	ds_read_b128 v[154:157], v210 offset:6144
	v_exp_f32_e32 v212, v202
	v_exp_f32_e32 v213, v203
	v_exp_f32_e32 v214, v204
	v_exp_f32_e32 v215, v205
	v_add_f32_e32 v224, 1.0, v224
	v_add_f32_e32 v225, 1.0, v225
	v_add_f32_e32 v226, 1.0, v226
	v_add_f32_e32 v227, 1.0, v227
	v_fmac_f32_e32 v224, v224, v212
	v_fmac_f32_e32 v225, v225, v213
	v_fmac_f32_e32 v226, v226, v214
	v_fmac_f32_e32 v227, v227, v215
	v_mfma_f32_32x32x16_bf16 v[82:97], v[50:53], v[190:193], v[82:97]
	ds_read_b128 v[158:161], v210 offset:7168
	v_rcp_f32_e32 v224, v224
	v_rcp_f32_e32 v225, v225
	v_rcp_f32_e32 v226, v226
	v_rcp_f32_e32 v227, v227
	v_fma_f32 v224, -v212, v224, v224
	v_fma_f32 v225, -v213, v225, v225
	v_fma_f32 v226, -v214, v226, v226
	v_fma_f32 v227, -v215, v227, v227
	v_cvt_pk_bf16_f32 v224, v224, v225
	v_cvt_pk_bf16_f32 v225, v226, v227
	ds_write_b64 v211, v[224:225] offset:8192
	s_waitcnt lgkmcnt(1)
	v_mfma_f32_32x32x16_bf16 v[2:17], v[126:129], v[130:133], v[2:17]
	v_add_u32_e32 v234, v231, v245
	ds_read_b128 v[34:37], v234 offset:0
	ds_read_b128 v[38:41], v234 offset:16
	ds_read_b128 v[42:45], v234 offset:32
	ds_read_b128 v[46:49], v234 offset:48
	v_add_u32_e32 v232, 0x100, v232
	v_exp_f32_e32 v212, v84
	v_exp_f32_e32 v213, v88
	v_exp_f32_e32 v214, v92
	v_exp_f32_e32 v215, v96
	v_mfma_f32_32x32x16_bf16 v[2:17], v[122:125], v[134:137], v[2:17]
	v_exp_f32_e32 v216, v82
	v_exp_f32_e32 v217, v86
	v_exp_f32_e32 v218, v90
	v_exp_f32_e32 v219, v94
	v_add_f32_e32 v236, 1.0, v212
	v_add_f32_e32 v237, 1.0, v213
	v_add_f32_e32 v238, 1.0, v214
	v_add_f32_e32 v239, 1.0, v215
	v_fma_f32 v240, v212, s12, v235
	v_fma_f32 v241, v213, s12, v235
	v_fma_f32 v242, v214, s12, v235
	v_fma_f32 v243, v215, s12, v235
	v_mfma_f32_32x32x16_bf16 v[2:17], v[118:121], v[138:141], v[2:17]
	v_exp_f32_e32 v220, v83
	v_exp_f32_e32 v221, v87
	v_exp_f32_e32 v222, v91
	v_exp_f32_e32 v223, v95
	v_fmac_f32_e32 v236, v216, v236
	v_fmac_f32_e32 v237, v217, v237
	v_fmac_f32_e32 v238, v218, v238
	v_fmac_f32_e32 v239, v219, v239
	v_mfma_f32_32x32x16_bf16 v[2:17], v[114:117], v[142:145], v[2:17]
	v_rcp_f32_e32 v216, v236
	v_rcp_f32_e32 v217, v237
	v_rcp_f32_e32 v218, v238
	v_rcp_f32_e32 v219, v239
	v_add_f32_e32 v220, 1.0, v220
	v_add_f32_e32 v221, 1.0, v221
	v_add_f32_e32 v222, 1.0, v222
	v_add_f32_e32 v223, 1.0, v223
	v_mfma_f32_32x32x16_bf16 v[2:17], v[110:113], v[146:149], v[2:17]
	v_rcp_f32_e32 v220, v220
	v_rcp_f32_e32 v221, v221
	v_rcp_f32_e32 v222, v222
	v_rcp_f32_e32 v223, v223
	v_mul_f32_e32 v240, v240, v216
	v_mul_f32_e32 v241, v241, v217
	v_mul_f32_e32 v242, v242, v218
	v_mul_f32_e32 v243, v243, v219
	v_mfma_f32_32x32x16_bf16 v[2:17], v[106:109], v[150:153], v[2:17]
	v_exp_f32_e32 v224, v85
	v_exp_f32_e32 v225, v89
	v_exp_f32_e32 v226, v93
	v_exp_f32_e32 v227, v97
	v_fma_f32 v206, v220, v206, v240
	v_fma_f32 v207, v221, v207, v241
	v_fma_f32 v208, v222, v208, v242
	v_fma_f32 v209, v223, v209, v243
	v_mfma_f32_32x32x16_bf16 v[2:17], v[102:105], v[154:157], v[2:17]
	v_exp_f32_e32 v212, v206
	v_exp_f32_e32 v213, v207
	v_exp_f32_e32 v214, v208
	v_exp_f32_e32 v215, v209
	v_add_f32_e32 v224, 1.0, v224
	v_add_f32_e32 v225, 1.0, v225
	v_add_f32_e32 v226, 1.0, v226
	v_add_f32_e32 v227, 1.0, v227
	v_fmac_f32_e32 v224, v224, v212
	v_fmac_f32_e32 v225, v225, v213
	v_fmac_f32_e32 v226, v226, v214
	v_fmac_f32_e32 v227, v227, v215
	v_mfma_f32_32x32x16_bf16 v[2:17], v[98:101], v[158:161], v[2:17]
	v_rcp_f32_e32 v224, v224
	v_rcp_f32_e32 v225, v225
	v_rcp_f32_e32 v226, v226
	v_rcp_f32_e32 v227, v227
	v_fma_f32 v224, -v212, v224, v224
	v_fma_f32 v225, -v213, v225, v225
	v_fma_f32 v226, -v214, v226, v226
	v_fma_f32 v227, -v215, v227, v227
	v_cvt_pk_bf16_f32 v224, v224, v225
	v_cvt_pk_bf16_f32 v225, v226, v227
	ds_write_b64 v211, v[224:225] offset:8200
	s_waitcnt lgkmcnt(0)
	s_barrier
	s_sub_u32 s16, s16, 1
	s_cmp_lg_u32 s16, 0
	s_cbranch_scc1 .Llight_loop
	s_nop 7
	s_nop 7
	s_branch .Lepilogue

	.amdhsa_kernel _Z11lstm_kernelPKiPKhPKfS4_S4_Pf
		.amdhsa_group_segment_fixed_size 163840
		.amdhsa_private_segment_fixed_size 0
		.amdhsa_kernarg_size 48
		.amdhsa_user_sgpr_count 2
		.amdhsa_user_sgpr_dispatch_ptr 0
		.amdhsa_user_sgpr_queue_ptr 0
		.amdhsa_user_sgpr_kernarg_segment_ptr 1
		.amdhsa_user_sgpr_dispatch_id 0
		.amdhsa_user_sgpr_kernarg_preload_length 0
		.amdhsa_user_sgpr_kernarg_preload_offset 0
		.amdhsa_user_sgpr_private_segment_size 0
		.amdhsa_uses_dynamic_stack 0
		.amdhsa_enable_private_segment 0
		.amdhsa_system_sgpr_workgroup_id_x 1
		.amdhsa_system_sgpr_workgroup_id_y 0
		.amdhsa_system_sgpr_workgroup_id_z 0
		.amdhsa_system_sgpr_workgroup_info 0
		.amdhsa_system_vgpr_workitem_id 0
		.amdhsa_next_free_vgpr 246
		.amdhsa_next_free_sgpr 91
		.amdhsa_accum_offset 248
		.amdhsa_reserve_vcc 1
		.amdhsa_float_round_mode_32 0
		.amdhsa_float_round_mode_16_64 0
		.amdhsa_float_denorm_mode_32 3
		.amdhsa_float_denorm_mode_16_64 3
		.amdhsa_dx10_clamp 1
		.amdhsa_ieee_mode 1
		.amdhsa_fp16_overflow 0
		.amdhsa_tg_split 0
		.amdhsa_exception_fp_ieee_invalid_op 0
		.amdhsa_exception_fp_denorm_src 0
		.amdhsa_exception_fp_ieee_div_zero 0
		.amdhsa_exception_fp_ieee_overflow 0
		.amdhsa_exception_fp_ieee_underflow 0
		.amdhsa_exception_fp_ieee_inexact 0
		.amdhsa_exception_int_div_zero 0
	.end_amdhsa_kernel

amdhsa.kernels:
  - .agpr_count:     0
    .args:
      - .actual_access:  read_only
        .address_space:  global
        .offset:         0
        .size:           8
        .value_kind:     global_buffer
      - .actual_access:  read_only
        .address_space:  global
        .offset:         8
        .size:           8
        .value_kind:     global_buffer
      - .actual_access:  read_only
        .address_space:  global
        .offset:         16
        .size:           8
        .value_kind:     global_buffer
      - .actual_access:  read_only
        .address_space:  global
        .offset:         24
        .size:           8
        .value_kind:     global_buffer
      - .actual_access:  read_only
        .address_space:  global
        .offset:         32
        .size:           8
        .value_kind:     global_buffer
      - .actual_access:  read_only
        .address_space:  global
        .offset:         40
        .size:           8
        .value_kind:     global_buffer
      - .actual_access:  write_only
        .address_space:  global
        .offset:         48
        .size:           8
        .value_kind:     global_buffer
      - .offset:         56
        .size:           4
        .value_kind:     hidden_block_count_x
      - .offset:         60
        .size:           4
        .value_kind:     hidden_block_count_y
      - .offset:         64
        .size:           4
        .value_kind:     hidden_block_count_z
      - .offset:         68
        .size:           2
        .value_kind:     hidden_group_size_x
      - .offset:         70
        .size:           2
        .value_kind:     hidden_group_size_y
      - .offset:         72
        .size:           2
        .value_kind:     hidden_group_size_z
      - .offset:         74
        .size:           2
        .value_kind:     hidden_remainder_x
      - .offset:         76
        .size:           2
        .value_kind:     hidden_remainder_y
      - .offset:         78
        .size:           2
        .value_kind:     hidden_remainder_z
      - .offset:         96
        .size:           8
        .value_kind:     hidden_global_offset_x
      - .offset:         104
        .size:           8
        .value_kind:     hidden_global_offset_y
      - .offset:         112
        .size:           8
        .value_kind:     hidden_global_offset_z
      - .offset:         120
        .size:           2
        .value_kind:     hidden_grid_dims
    .group_segment_fixed_size: 0
    .kernarg_segment_align: 8
    .kernarg_segment_size: 312
    .language:       OpenCL C
    .language_version:
      - 2
      - 0
    .max_flat_workgroup_size: 1024
    .name:           _Z11prep_kernelPKfS0_S0_S0_S0_S0_Ph
    .private_segment_fixed_size: 0
    .sgpr_count:     22
    .sgpr_spill_count: 0
    .symbol:         _Z11prep_kernelPKfS0_S0_S0_S0_S0_Ph.kd
    .uniform_work_group_size: 1
    .uses_dynamic_stack: false
    .vgpr_count:     20
    .vgpr_spill_count: 0
    .wavefront_size: 64
  - .agpr_count:     0
    .args:
      - .actual_access:  read_only
        .address_space:  global
        .offset:         0
        .size:           8
        .value_kind:     global_buffer
      - .actual_access:  read_only
        .address_space:  global
        .offset:         8
        .size:           8
        .value_kind:     global_buffer
      - .actual_access:  read_only
        .address_space:  global
        .offset:         16
        .size:           8
        .value_kind:     global_buffer
      - .actual_access:  read_only
        .address_space:  global
        .offset:         24
        .size:           8
        .value_kind:     global_buffer
      - .actual_access:  read_only
        .address_space:  global
        .offset:         32
        .size:           8
        .value_kind:     global_buffer
      - .actual_access:  write_only
        .address_space:  global
        .offset:         40
        .size:           8
        .value_kind:     global_buffer
    .group_segment_fixed_size: 163840
    .kernarg_segment_align: 8
    .kernarg_segment_size: 48
    .language:       OpenCL C
    .language_version:
      - 2
      - 0
    .max_flat_workgroup_size: 512
    .name:           _Z11lstm_kernelPKiPKhPKfS4_S4_Pf
    .private_segment_fixed_size: 0
    .sgpr_count:     26
    .sgpr_spill_count: 0
    .symbol:         _Z11lstm_kernelPKiPKhPKfS4_S4_Pf.kd
    .uniform_work_group_size: 1
    .uses_dynamic_stack: false
    .vgpr_count:     246
    .vgpr_spill_count: 0
    .wavefront_size: 64
